# cache policy: nt on routed-expert weight loads; write-through (sc0 sc1) stores for the QKV epilogue and the attention merge outputs
# speedup vs baseline: 1.0210x; 1.0210x over previous
.LBB0_129:
	s_lshl_b32 s12, s12, 8
	s_add_i32 s12, s12, s69
	v_or_b32_e32 v2, s12, v3
	s_lshl_b32 s8, s8, 8
	v_mul_lo_u32 v2, v2, s2
	s_or_b32 s8, s8, s67
	v_add_u32_e32 v2, s8, v2
	s_mov_b64 s[40:41], s[14:15]
	v_add_lshl_u32 v0, v2, v0, 1
	v_cvt_pk_bf16_f32 v2, v142, v143
	v_mov_b32_e32 v6, v0
	v_cvt_pk_bf16_f32 v3, v144, v145
	v_cvt_pk_bf16_f32 v4, v138, v139
	v_cvt_pk_bf16_f32 v5, v140, v141
	global_store_dwordx4 v6, v[2:5], s[40:41] sc0 sc1
	v_add_u32_e32 v0, s59, v0
	s_mul_i32 s8, s2, 0xa0
	v_cvt_pk_bf16_f32 v2, v126, v127
	v_cvt_pk_bf16_f32 v3, v128, v129
	v_cvt_pk_bf16_f32 v4, v122, v123
	v_cvt_pk_bf16_f32 v5, v124, v125
	global_store_dwordx4 v6, v[2:5], s[40:41] offset:256 sc0 sc1
	v_mov_b32_e32 v6, v0
	v_add_u32_e32 v0, s59, v0
	v_cvt_pk_bf16_f32 v2, v134, v135
	v_cvt_pk_bf16_f32 v3, v136, v137
	v_cvt_pk_bf16_f32 v4, v130, v131
	v_cvt_pk_bf16_f32 v5, v132, v133
	global_store_dwordx4 v6, v[2:5], s[40:41] sc0 sc1
	s_and_b64 vcc, exec, s[38:39]
	s_mov_b32 s12, s30
	v_cvt_pk_bf16_f32 v2, v110, v111
	v_cvt_pk_bf16_f32 v3, v112, v113
	v_cvt_pk_bf16_f32 v4, v106, v107
	v_cvt_pk_bf16_f32 v5, v108, v109
	global_store_dwordx4 v6, v[2:5], s[40:41] offset:256 sc0 sc1
	v_mov_b32_e32 v6, v0
	v_add_u32_e32 v0, s59, v0
	v_cvt_pk_bf16_f32 v2, v118, v119
	v_cvt_pk_bf16_f32 v3, v120, v121
	v_cvt_pk_bf16_f32 v4, v114, v115
	v_cvt_pk_bf16_f32 v5, v116, v117
	global_store_dwordx4 v6, v[2:5], s[40:41] sc0 sc1
	s_mov_b64 s[42:43], s[36:37]
	s_nop 0
	v_cvt_pk_bf16_f32 v2, v94, v95
	v_cvt_pk_bf16_f32 v3, v96, v97
	v_cvt_pk_bf16_f32 v4, v90, v91
	v_cvt_pk_bf16_f32 v5, v92, v93
	global_store_dwordx4 v6, v[2:5], s[40:41] offset:256 sc0 sc1
	v_mov_b32_e32 v6, v0
	v_add_u32_e32 v0, s8, v0
	v_cvt_pk_bf16_f32 v2, v102, v103
	v_cvt_pk_bf16_f32 v3, v104, v105
	v_cvt_pk_bf16_f32 v4, v98, v99
	v_cvt_pk_bf16_f32 v5, v100, v101
	global_store_dwordx4 v6, v[2:5], s[40:41] sc0 sc1
	s_mov_b32 s8, s18
	s_nop 0
	v_cvt_pk_bf16_f32 v2, v86, v87
	v_cvt_pk_bf16_f32 v3, v88, v89
	v_cvt_pk_bf16_f32 v4, v82, v83
	v_cvt_pk_bf16_f32 v5, v84, v85
	global_store_dwordx4 v6, v[2:5], s[40:41] offset:256 sc0 sc1
	v_mov_b32_e32 v6, v0
	v_add_u32_e32 v0, s59, v0
	v_cvt_pk_bf16_f32 v2, v78, v79
	v_cvt_pk_bf16_f32 v3, v80, v81
	v_cvt_pk_bf16_f32 v4, v74, v75
	v_cvt_pk_bf16_f32 v5, v76, v77
	global_store_dwordx4 v6, v[2:5], s[40:41] sc0 sc1
	s_nop 1
	v_cvt_pk_bf16_f32 v2, v62, v63
	v_cvt_pk_bf16_f32 v3, v64, v65
	v_cvt_pk_bf16_f32 v4, v58, v59
	v_cvt_pk_bf16_f32 v5, v60, v61
	global_store_dwordx4 v6, v[2:5], s[40:41] offset:256 sc0 sc1
	v_mov_b32_e32 v6, v0
	v_add_u32_e32 v0, s59, v0
	v_cvt_pk_bf16_f32 v2, v70, v71
	v_cvt_pk_bf16_f32 v3, v72, v73
	v_cvt_pk_bf16_f32 v4, v66, v67
	v_cvt_pk_bf16_f32 v5, v68, v69
	global_store_dwordx4 v6, v[2:5], s[40:41] sc0 sc1
	s_nop 1
	v_cvt_pk_bf16_f32 v2, v46, v47
	v_cvt_pk_bf16_f32 v3, v48, v49
	v_cvt_pk_bf16_f32 v4, v42, v43
	v_cvt_pk_bf16_f32 v5, v44, v45
	global_store_dwordx4 v6, v[2:5], s[40:41] offset:256 sc0 sc1
	v_mov_b32_e32 v6, v0
	v_add_u32_e32 v0, s59, v0
	v_cvt_pk_bf16_f32 v2, v54, v55
	v_cvt_pk_bf16_f32 v3, v56, v57
	v_cvt_pk_bf16_f32 v4, v50, v51
	v_cvt_pk_bf16_f32 v5, v52, v53
	global_store_dwordx4 v6, v[2:5], s[40:41] sc0 sc1
	s_nop 1
	v_cvt_pk_bf16_f32 v2, v30, v31
	v_cvt_pk_bf16_f32 v3, v32, v33
	v_cvt_pk_bf16_f32 v4, v26, v27
	v_cvt_pk_bf16_f32 v5, v28, v29
	global_store_dwordx4 v6, v[2:5], s[40:41] offset:256 sc0 sc1
	s_nop 1
	v_cvt_pk_bf16_f32 v2, v38, v39
	v_cvt_pk_bf16_f32 v3, v40, v41
	v_cvt_pk_bf16_f32 v4, v34, v35
	v_cvt_pk_bf16_f32 v5, v36, v37
	global_store_dwordx4 v0, v[2:5], s[40:41] sc0 sc1
	s_nop 1
	v_cvt_pk_bf16_f32 v2, v22, v23
	v_cvt_pk_bf16_f32 v3, v24, v25
	v_cvt_pk_bf16_f32 v4, v18, v19
	v_cvt_pk_bf16_f32 v5, v20, v21
	global_store_dwordx4 v0, v[2:5], s[40:41] offset:256 sc0 sc1
	s_mov_b64 s[40:41], s[34:35]
	s_cbranch_vccnz .LBB0_169

.Lmg1_loop:
	v_add_u32_e32 v193, s45, v2
	v_min_u32_e32 v193, s43, v193
	v_lshrrev_b32_e32 v6, 1, v193
	v_lshlrev_b32_e32 v7, 4, v193
	v_and_b32_e32 v6, -4, v6
	global_load_dwordx4 v[194:197], v7, s[14:15]
	global_load_dwordx4 v[198:201], v7, s[16:17]
	global_load_dwordx4 v[202:205], v7, s[18:19]
	global_load_dword v190, v6, s[12:13]
	global_load_dword v191, v6, s[38:39]
	global_load_dword v192, v6, s[40:41]
	v_add_u32_e32 v209, s46, v2
	v_min_u32_e32 v209, s43, v209
	v_lshrrev_b32_e32 v6, 1, v209
	v_lshlrev_b32_e32 v7, 4, v209
	v_and_b32_e32 v6, -4, v6
	global_load_dwordx4 v[210:213], v7, s[14:15]
	global_load_dwordx4 v[214:217], v7, s[16:17]
	global_load_dwordx4 v[238:241], v7, s[18:19]
	global_load_dword v206, v6, s[12:13]
	global_load_dword v207, v6, s[38:39]
	global_load_dword v208, v6, s[40:41]
	s_waitcnt vmcnt(12)
	v_max3_f32 v8, v32, v33, v34
	v_sub_f32_e32 v9, v32, v8
	v_mul_f32_e32 v13, 0x3fb8aa3b, v9
	v_fma_f32 v14, v9, s94, -v13
	v_rndne_f32_e32 v15, v13
	v_fmac_f32_e32 v14, 0x32a5705f, v9
	v_sub_f32_e32 v13, v13, v15
	v_add_f32_e32 v13, v13, v14
	v_exp_f32_e32 v10, v13
	v_cvt_i32_f32_e32 v15, v15
	v_cmp_ngt_f32_e32 vcc, s95, v9
	v_ldexp_f32 v10, v10, v15
	s_nop 1
	v_cndmask_b32_e32 v10, 0, v10, vcc
	v_cmp_nlt_f32_e32 vcc, s96, v9
	s_nop 1
	v_cndmask_b32_e32 v10, v227, v10, vcc
	v_sub_f32_e32 v9, v33, v8
	v_mul_f32_e32 v13, 0x3fb8aa3b, v9
	v_fma_f32 v14, v9, s94, -v13
	v_rndne_f32_e32 v15, v13
	v_fmac_f32_e32 v14, 0x32a5705f, v9
	v_sub_f32_e32 v13, v13, v15
	v_add_f32_e32 v13, v13, v14
	v_exp_f32_e32 v11, v13
	v_cvt_i32_f32_e32 v15, v15
	v_cmp_ngt_f32_e32 vcc, s95, v9
	v_ldexp_f32 v11, v11, v15
	s_nop 1
	v_cndmask_b32_e32 v11, 0, v11, vcc
	v_cmp_nlt_f32_e32 vcc, s96, v9
	s_nop 1
	v_cndmask_b32_e32 v11, v227, v11, vcc
	v_sub_f32_e32 v9, v34, v8
	v_mul_f32_e32 v13, 0x3fb8aa3b, v9
	v_fma_f32 v14, v9, s94, -v13
	v_rndne_f32_e32 v15, v13
	v_fmac_f32_e32 v14, 0x32a5705f, v9
	v_sub_f32_e32 v13, v13, v15
	v_add_f32_e32 v13, v13, v14
	v_exp_f32_e32 v12, v13
	v_cvt_i32_f32_e32 v15, v15
	v_cmp_ngt_f32_e32 vcc, s95, v9
	v_ldexp_f32 v12, v12, v15
	s_nop 1
	v_cndmask_b32_e32 v12, 0, v12, vcc
	v_cmp_nlt_f32_e32 vcc, s96, v9
	s_nop 1
	v_cndmask_b32_e32 v12, v227, v12, vcc
	v_add_f32_e32 v16, v10, v11
	v_add_f32_e32 v16, v12, v16
	v_div_scale_f32 v17, s[2:3], v16, v16, 1.0
	v_rcp_f32_e32 v18, v17
	s_nop 0
	v_fma_f32 v19, -v17, v18, 1.0
	v_fmac_f32_e32 v18, v19, v18
	v_div_scale_f32 v20, vcc, 1.0, v16, 1.0
	v_mul_f32_e32 v21, v20, v18
	v_fma_f32 v22, -v17, v21, v20
	v_fmac_f32_e32 v21, v22, v18
	v_fma_f32 v17, -v17, v21, v20
	v_div_fmas_f32 v17, v17, v18, v21
	v_div_fixup_f32 v16, v17, v16, 1.0
	v_mul_f32_e32 v16, 0x41800000, v16
	v_mul_f32_e32 v10, v10, v16
	v_mul_f32_e32 v11, v11, v16
	v_mul_f32_e32 v12, v12, v16
	v_lshlrev_b32_e32 v13, 16, v36
	v_and_b32_e32 v14, 0xffff0000, v36
	v_mul_f32_e32 v20, v10, v13
	v_mul_f32_e32 v21, v10, v14
	v_lshlrev_b32_e32 v13, 16, v40
	v_and_b32_e32 v14, 0xffff0000, v40
	v_fmac_f32_e32 v20, v11, v13
	v_fmac_f32_e32 v21, v11, v14
	v_lshlrev_b32_e32 v13, 16, v44
	v_and_b32_e32 v14, 0xffff0000, v44
	v_fmac_f32_e32 v20, v12, v13
	v_fmac_f32_e32 v21, v12, v14
	v_lshlrev_b32_e32 v13, 16, v37
	v_and_b32_e32 v14, 0xffff0000, v37
	v_mul_f32_e32 v22, v10, v13
	v_mul_f32_e32 v23, v10, v14
	v_lshlrev_b32_e32 v13, 16, v41
	v_and_b32_e32 v14, 0xffff0000, v41
	v_fmac_f32_e32 v22, v11, v13
	v_fmac_f32_e32 v23, v11, v14
	v_lshlrev_b32_e32 v13, 16, v45
	v_and_b32_e32 v14, 0xffff0000, v45
	v_fmac_f32_e32 v22, v12, v13
	v_fmac_f32_e32 v23, v12, v14
	v_lshlrev_b32_e32 v13, 16, v38
	v_and_b32_e32 v14, 0xffff0000, v38
	v_mul_f32_e32 v24, v10, v13
	v_mul_f32_e32 v25, v10, v14
	v_lshlrev_b32_e32 v13, 16, v42
	v_and_b32_e32 v14, 0xffff0000, v42
	v_fmac_f32_e32 v24, v11, v13
	v_fmac_f32_e32 v25, v11, v14
	v_lshlrev_b32_e32 v13, 16, v46
	v_and_b32_e32 v14, 0xffff0000, v46
	v_fmac_f32_e32 v24, v12, v13
	v_fmac_f32_e32 v25, v12, v14
	v_lshlrev_b32_e32 v13, 16, v39
	v_and_b32_e32 v14, 0xffff0000, v39
	v_mul_f32_e32 v26, v10, v13
	v_mul_f32_e32 v27, v10, v14
	v_lshlrev_b32_e32 v13, 16, v43
	v_and_b32_e32 v14, 0xffff0000, v43
	v_fmac_f32_e32 v26, v11, v13
	v_fmac_f32_e32 v27, v11, v14
	v_lshlrev_b32_e32 v13, 16, v47
	v_and_b32_e32 v14, 0xffff0000, v47
	v_fmac_f32_e32 v26, v12, v13
	v_fmac_f32_e32 v27, v12, v14
	v_mov_b32_e32 v16, 0
	v_mov_b32_e32 v17, 0
	v_lshlrev_b32_e32 v7, 3, v35
	v_cvt_pk_fp8_f32 v16, v20, v21
	v_cvt_pk_fp8_f32 v17, v24, v25
	s_nop 0
	v_cvt_pk_fp8_f32 v16, v22, v23 op_sel:[0,0,1]
	v_cvt_pk_fp8_f32 v17, v26, v27 op_sel:[0,0,1]
	s_nop 0
	global_store_dwordx2 v7, v[16:17], s[30:31] sc0 sc1
	v_max3_f32 v8, v48, v49, v50
	v_sub_f32_e32 v9, v48, v8
	v_mul_f32_e32 v13, 0x3fb8aa3b, v9
	v_fma_f32 v14, v9, s94, -v13
	v_rndne_f32_e32 v15, v13
	v_fmac_f32_e32 v14, 0x32a5705f, v9
	v_sub_f32_e32 v13, v13, v15
	v_add_f32_e32 v13, v13, v14
	v_exp_f32_e32 v10, v13
	v_cvt_i32_f32_e32 v15, v15
	v_cmp_ngt_f32_e32 vcc, s95, v9
	v_ldexp_f32 v10, v10, v15
	s_nop 1
	v_cndmask_b32_e32 v10, 0, v10, vcc
	v_cmp_nlt_f32_e32 vcc, s96, v9
	s_nop 1
	v_cndmask_b32_e32 v10, v227, v10, vcc
	v_sub_f32_e32 v9, v49, v8
	v_mul_f32_e32 v13, 0x3fb8aa3b, v9
	v_fma_f32 v14, v9, s94, -v13
	v_rndne_f32_e32 v15, v13
	v_fmac_f32_e32 v14, 0x32a5705f, v9
	v_sub_f32_e32 v13, v13, v15
	v_add_f32_e32 v13, v13, v14
	v_exp_f32_e32 v11, v13
	v_cvt_i32_f32_e32 v15, v15
	v_cmp_ngt_f32_e32 vcc, s95, v9
	v_ldexp_f32 v11, v11, v15
	s_nop 1
	v_cndmask_b32_e32 v11, 0, v11, vcc
	v_cmp_nlt_f32_e32 vcc, s96, v9
	s_nop 1
	v_cndmask_b32_e32 v11, v227, v11, vcc
	v_sub_f32_e32 v9, v50, v8
	v_mul_f32_e32 v13, 0x3fb8aa3b, v9
	v_fma_f32 v14, v9, s94, -v13
	v_rndne_f32_e32 v15, v13
	v_fmac_f32_e32 v14, 0x32a5705f, v9
	v_sub_f32_e32 v13, v13, v15
	v_add_f32_e32 v13, v13, v14
	v_exp_f32_e32 v12, v13
	v_cvt_i32_f32_e32 v15, v15
	v_cmp_ngt_f32_e32 vcc, s95, v9
	v_ldexp_f32 v12, v12, v15
	s_nop 1
	v_cndmask_b32_e32 v12, 0, v12, vcc
	v_cmp_nlt_f32_e32 vcc, s96, v9
	s_nop 1
	v_cndmask_b32_e32 v12, v227, v12, vcc
	v_add_f32_e32 v16, v10, v11
	v_add_f32_e32 v16, v12, v16
	v_div_scale_f32 v17, s[2:3], v16, v16, 1.0
	v_rcp_f32_e32 v18, v17
	s_nop 0
	v_fma_f32 v19, -v17, v18, 1.0
	v_fmac_f32_e32 v18, v19, v18
	v_div_scale_f32 v20, vcc, 1.0, v16, 1.0
	v_mul_f32_e32 v21, v20, v18
	v_fma_f32 v22, -v17, v21, v20
	v_fmac_f32_e32 v21, v22, v18
	v_fma_f32 v17, -v17, v21, v20
	v_div_fmas_f32 v17, v17, v18, v21
	v_div_fixup_f32 v16, v17, v16, 1.0
	v_mul_f32_e32 v16, 0x41800000, v16
	v_mul_f32_e32 v10, v10, v16
	v_mul_f32_e32 v11, v11, v16
	v_mul_f32_e32 v12, v12, v16
	v_lshlrev_b32_e32 v13, 16, v52
	v_and_b32_e32 v14, 0xffff0000, v52
	v_mul_f32_e32 v20, v10, v13
	v_mul_f32_e32 v21, v10, v14
	v_lshlrev_b32_e32 v13, 16, v56
	v_and_b32_e32 v14, 0xffff0000, v56
	v_fmac_f32_e32 v20, v11, v13
	v_fmac_f32_e32 v21, v11, v14
	v_lshlrev_b32_e32 v13, 16, v60
	v_and_b32_e32 v14, 0xffff0000, v60
	v_fmac_f32_e32 v20, v12, v13
	v_fmac_f32_e32 v21, v12, v14
	v_lshlrev_b32_e32 v13, 16, v53
	v_and_b32_e32 v14, 0xffff0000, v53
	v_mul_f32_e32 v22, v10, v13
	v_mul_f32_e32 v23, v10, v14
	v_lshlrev_b32_e32 v13, 16, v57
	v_and_b32_e32 v14, 0xffff0000, v57
	v_fmac_f32_e32 v22, v11, v13
	v_fmac_f32_e32 v23, v11, v14
	v_lshlrev_b32_e32 v13, 16, v61
	v_and_b32_e32 v14, 0xffff0000, v61
	v_fmac_f32_e32 v22, v12, v13
	v_fmac_f32_e32 v23, v12, v14
	v_lshlrev_b32_e32 v13, 16, v54
	v_and_b32_e32 v14, 0xffff0000, v54
	v_mul_f32_e32 v24, v10, v13
	v_mul_f32_e32 v25, v10, v14
	v_lshlrev_b32_e32 v13, 16, v58
	v_and_b32_e32 v14, 0xffff0000, v58
	v_fmac_f32_e32 v24, v11, v13
	v_fmac_f32_e32 v25, v11, v14
	v_lshlrev_b32_e32 v13, 16, v62
	v_and_b32_e32 v14, 0xffff0000, v62
	v_fmac_f32_e32 v24, v12, v13
	v_fmac_f32_e32 v25, v12, v14
	v_lshlrev_b32_e32 v13, 16, v55
	v_and_b32_e32 v14, 0xffff0000, v55
	v_mul_f32_e32 v26, v10, v13
	v_mul_f32_e32 v27, v10, v14
	v_lshlrev_b32_e32 v13, 16, v59
	v_and_b32_e32 v14, 0xffff0000, v59
	v_fmac_f32_e32 v26, v11, v13
	v_fmac_f32_e32 v27, v11, v14
	v_lshlrev_b32_e32 v13, 16, v63
	v_and_b32_e32 v14, 0xffff0000, v63
	v_fmac_f32_e32 v26, v12, v13
	v_fmac_f32_e32 v27, v12, v14
	v_mov_b32_e32 v16, 0
	v_mov_b32_e32 v17, 0
	v_lshlrev_b32_e32 v7, 3, v51
	v_cvt_pk_fp8_f32 v16, v20, v21
	v_cvt_pk_fp8_f32 v17, v24, v25
	s_nop 0
	v_cvt_pk_fp8_f32 v16, v22, v23 op_sel:[0,0,1]
	v_cvt_pk_fp8_f32 v17, v26, v27 op_sel:[0,0,1]
	s_nop 0
	global_store_dwordx2 v7, v[16:17], s[30:31] sc0 sc1
	v_add_u32_e32 v2, s47, v2
	s_add_u32 s44, s44, s47
	v_min_u32_e32 v35, s43, v2
	v_lshrrev_b32_e32 v6, 1, v35
	v_lshlrev_b32_e32 v7, 4, v35
	v_and_b32_e32 v6, -4, v6
	global_load_dwordx4 v[36:39], v7, s[14:15]
	global_load_dwordx4 v[40:43], v7, s[16:17]
	global_load_dwordx4 v[44:47], v7, s[18:19]
	global_load_dword v32, v6, s[12:13]
	global_load_dword v33, v6, s[38:39]
	global_load_dword v34, v6, s[40:41]
	v_add_u32_e32 v51, s42, v2
	v_min_u32_e32 v51, s43, v51
	v_lshrrev_b32_e32 v6, 1, v51
	v_lshlrev_b32_e32 v7, 4, v51
	v_and_b32_e32 v6, -4, v6
	global_load_dwordx4 v[52:55], v7, s[14:15]
	global_load_dwordx4 v[56:59], v7, s[16:17]
	global_load_dwordx4 v[60:63], v7, s[18:19]
	global_load_dword v48, v6, s[12:13]
	global_load_dword v49, v6, s[38:39]
	global_load_dword v50, v6, s[40:41]
	s_waitcnt vmcnt(12)
	v_max3_f32 v8, v190, v191, v192
	v_sub_f32_e32 v9, v190, v8
	v_mul_f32_e32 v13, 0x3fb8aa3b, v9
	v_fma_f32 v14, v9, s94, -v13
	v_rndne_f32_e32 v15, v13
	v_fmac_f32_e32 v14, 0x32a5705f, v9
	v_sub_f32_e32 v13, v13, v15
	v_add_f32_e32 v13, v13, v14
	v_exp_f32_e32 v10, v13
	v_cvt_i32_f32_e32 v15, v15
	v_cmp_ngt_f32_e32 vcc, s95, v9
	v_ldexp_f32 v10, v10, v15
	s_nop 1
	v_cndmask_b32_e32 v10, 0, v10, vcc
	v_cmp_nlt_f32_e32 vcc, s96, v9
	s_nop 1
	v_cndmask_b32_e32 v10, v227, v10, vcc
	v_sub_f32_e32 v9, v191, v8
	v_mul_f32_e32 v13, 0x3fb8aa3b, v9
	v_fma_f32 v14, v9, s94, -v13
	v_rndne_f32_e32 v15, v13
	v_fmac_f32_e32 v14, 0x32a5705f, v9
	v_sub_f32_e32 v13, v13, v15
	v_add_f32_e32 v13, v13, v14
	v_exp_f32_e32 v11, v13
	v_cvt_i32_f32_e32 v15, v15
	v_cmp_ngt_f32_e32 vcc, s95, v9
	v_ldexp_f32 v11, v11, v15
	s_nop 1
	v_cndmask_b32_e32 v11, 0, v11, vcc
	v_cmp_nlt_f32_e32 vcc, s96, v9
	s_nop 1
	v_cndmask_b32_e32 v11, v227, v11, vcc
	v_sub_f32_e32 v9, v192, v8
	v_mul_f32_e32 v13, 0x3fb8aa3b, v9
	v_fma_f32 v14, v9, s94, -v13
	v_rndne_f32_e32 v15, v13
	v_fmac_f32_e32 v14, 0x32a5705f, v9
	v_sub_f32_e32 v13, v13, v15
	v_add_f32_e32 v13, v13, v14
	v_exp_f32_e32 v12, v13
	v_cvt_i32_f32_e32 v15, v15
	v_cmp_ngt_f32_e32 vcc, s95, v9
	v_ldexp_f32 v12, v12, v15
	s_nop 1
	v_cndmask_b32_e32 v12, 0, v12, vcc
	v_cmp_nlt_f32_e32 vcc, s96, v9
	s_nop 1
	v_cndmask_b32_e32 v12, v227, v12, vcc
	v_add_f32_e32 v16, v10, v11
	v_add_f32_e32 v16, v12, v16
	v_div_scale_f32 v17, s[2:3], v16, v16, 1.0
	v_rcp_f32_e32 v18, v17
	s_nop 0
	v_fma_f32 v19, -v17, v18, 1.0
	v_fmac_f32_e32 v18, v19, v18
	v_div_scale_f32 v20, vcc, 1.0, v16, 1.0
	v_mul_f32_e32 v21, v20, v18
	v_fma_f32 v22, -v17, v21, v20
	v_fmac_f32_e32 v21, v22, v18
	v_fma_f32 v17, -v17, v21, v20
	v_div_fmas_f32 v17, v17, v18, v21
	v_div_fixup_f32 v16, v17, v16, 1.0
	v_mul_f32_e32 v16, 0x41800000, v16
	v_mul_f32_e32 v10, v10, v16
	v_mul_f32_e32 v11, v11, v16
	v_mul_f32_e32 v12, v12, v16
	v_lshlrev_b32_e32 v13, 16, v194
	v_and_b32_e32 v14, 0xffff0000, v194
	v_mul_f32_e32 v20, v10, v13
	v_mul_f32_e32 v21, v10, v14
	v_lshlrev_b32_e32 v13, 16, v198
	v_and_b32_e32 v14, 0xffff0000, v198
	v_fmac_f32_e32 v20, v11, v13
	v_fmac_f32_e32 v21, v11, v14
	v_lshlrev_b32_e32 v13, 16, v202
	v_and_b32_e32 v14, 0xffff0000, v202
	v_fmac_f32_e32 v20, v12, v13
	v_fmac_f32_e32 v21, v12, v14
	v_lshlrev_b32_e32 v13, 16, v195
	v_and_b32_e32 v14, 0xffff0000, v195
	v_mul_f32_e32 v22, v10, v13
	v_mul_f32_e32 v23, v10, v14
	v_lshlrev_b32_e32 v13, 16, v199
	v_and_b32_e32 v14, 0xffff0000, v199
	v_fmac_f32_e32 v22, v11, v13
	v_fmac_f32_e32 v23, v11, v14
	v_lshlrev_b32_e32 v13, 16, v203
	v_and_b32_e32 v14, 0xffff0000, v203
	v_fmac_f32_e32 v22, v12, v13
	v_fmac_f32_e32 v23, v12, v14
	v_lshlrev_b32_e32 v13, 16, v196
	v_and_b32_e32 v14, 0xffff0000, v196
	v_mul_f32_e32 v24, v10, v13
	v_mul_f32_e32 v25, v10, v14
	v_lshlrev_b32_e32 v13, 16, v200
	v_and_b32_e32 v14, 0xffff0000, v200
	v_fmac_f32_e32 v24, v11, v13
	v_fmac_f32_e32 v25, v11, v14
	v_lshlrev_b32_e32 v13, 16, v204
	v_and_b32_e32 v14, 0xffff0000, v204
	v_fmac_f32_e32 v24, v12, v13
	v_fmac_f32_e32 v25, v12, v14
	v_lshlrev_b32_e32 v13, 16, v197
	v_and_b32_e32 v14, 0xffff0000, v197
	v_mul_f32_e32 v26, v10, v13
	v_mul_f32_e32 v27, v10, v14
	v_lshlrev_b32_e32 v13, 16, v201
	v_and_b32_e32 v14, 0xffff0000, v201
	v_fmac_f32_e32 v26, v11, v13
	v_fmac_f32_e32 v27, v11, v14
	v_lshlrev_b32_e32 v13, 16, v205
	v_and_b32_e32 v14, 0xffff0000, v205
	v_fmac_f32_e32 v26, v12, v13
	v_fmac_f32_e32 v27, v12, v14
	v_mov_b32_e32 v16, 0
	v_mov_b32_e32 v17, 0
	v_lshlrev_b32_e32 v7, 3, v193
	v_cvt_pk_fp8_f32 v16, v20, v21
	v_cvt_pk_fp8_f32 v17, v24, v25
	s_nop 0
	v_cvt_pk_fp8_f32 v16, v22, v23 op_sel:[0,0,1]
	v_cvt_pk_fp8_f32 v17, v26, v27 op_sel:[0,0,1]
	s_nop 0
	global_store_dwordx2 v7, v[16:17], s[30:31] sc0 sc1
	v_max3_f32 v8, v206, v207, v208
	v_sub_f32_e32 v9, v206, v8
	v_mul_f32_e32 v13, 0x3fb8aa3b, v9
	v_fma_f32 v14, v9, s94, -v13
	v_rndne_f32_e32 v15, v13
	v_fmac_f32_e32 v14, 0x32a5705f, v9
	v_sub_f32_e32 v13, v13, v15
	v_add_f32_e32 v13, v13, v14
	v_exp_f32_e32 v10, v13
	v_cvt_i32_f32_e32 v15, v15
	v_cmp_ngt_f32_e32 vcc, s95, v9
	v_ldexp_f32 v10, v10, v15
	s_nop 1
	v_cndmask_b32_e32 v10, 0, v10, vcc
	v_cmp_nlt_f32_e32 vcc, s96, v9
	s_nop 1
	v_cndmask_b32_e32 v10, v227, v10, vcc
	v_sub_f32_e32 v9, v207, v8
	v_mul_f32_e32 v13, 0x3fb8aa3b, v9
	v_fma_f32 v14, v9, s94, -v13
	v_rndne_f32_e32 v15, v13
	v_fmac_f32_e32 v14, 0x32a5705f, v9
	v_sub_f32_e32 v13, v13, v15
	v_add_f32_e32 v13, v13, v14
	v_exp_f32_e32 v11, v13
	v_cvt_i32_f32_e32 v15, v15
	v_cmp_ngt_f32_e32 vcc, s95, v9
	v_ldexp_f32 v11, v11, v15
	s_nop 1
	v_cndmask_b32_e32 v11, 0, v11, vcc
	v_cmp_nlt_f32_e32 vcc, s96, v9
	s_nop 1
	v_cndmask_b32_e32 v11, v227, v11, vcc
	v_sub_f32_e32 v9, v208, v8
	v_mul_f32_e32 v13, 0x3fb8aa3b, v9
	v_fma_f32 v14, v9, s94, -v13
	v_rndne_f32_e32 v15, v13
	v_fmac_f32_e32 v14, 0x32a5705f, v9
	v_sub_f32_e32 v13, v13, v15
	v_add_f32_e32 v13, v13, v14
	v_exp_f32_e32 v12, v13
	v_cvt_i32_f32_e32 v15, v15
	v_cmp_ngt_f32_e32 vcc, s95, v9
	v_ldexp_f32 v12, v12, v15
	s_nop 1
	v_cndmask_b32_e32 v12, 0, v12, vcc
	v_cmp_nlt_f32_e32 vcc, s96, v9
	s_nop 1
	v_cndmask_b32_e32 v12, v227, v12, vcc
	v_add_f32_e32 v16, v10, v11
	v_add_f32_e32 v16, v12, v16
	v_div_scale_f32 v17, s[2:3], v16, v16, 1.0
	v_rcp_f32_e32 v18, v17
	s_nop 0
	v_fma_f32 v19, -v17, v18, 1.0
	v_fmac_f32_e32 v18, v19, v18
	v_div_scale_f32 v20, vcc, 1.0, v16, 1.0
	v_mul_f32_e32 v21, v20, v18
	v_fma_f32 v22, -v17, v21, v20
	v_fmac_f32_e32 v21, v22, v18
	v_fma_f32 v17, -v17, v21, v20
	v_div_fmas_f32 v17, v17, v18, v21
	v_div_fixup_f32 v16, v17, v16, 1.0
	v_mul_f32_e32 v16, 0x41800000, v16
	v_mul_f32_e32 v10, v10, v16
	v_mul_f32_e32 v11, v11, v16
	v_mul_f32_e32 v12, v12, v16
	v_lshlrev_b32_e32 v13, 16, v210
	v_and_b32_e32 v14, 0xffff0000, v210
	v_mul_f32_e32 v20, v10, v13
	v_mul_f32_e32 v21, v10, v14
	v_lshlrev_b32_e32 v13, 16, v214
	v_and_b32_e32 v14, 0xffff0000, v214
	v_fmac_f32_e32 v20, v11, v13
	v_fmac_f32_e32 v21, v11, v14
	v_lshlrev_b32_e32 v13, 16, v238
	v_and_b32_e32 v14, 0xffff0000, v238
	v_fmac_f32_e32 v20, v12, v13
	v_fmac_f32_e32 v21, v12, v14
	v_lshlrev_b32_e32 v13, 16, v211
	v_and_b32_e32 v14, 0xffff0000, v211
	v_mul_f32_e32 v22, v10, v13
	v_mul_f32_e32 v23, v10, v14
	v_lshlrev_b32_e32 v13, 16, v215
	v_and_b32_e32 v14, 0xffff0000, v215
	v_fmac_f32_e32 v22, v11, v13
	v_fmac_f32_e32 v23, v11, v14
	v_lshlrev_b32_e32 v13, 16, v239
	v_and_b32_e32 v14, 0xffff0000, v239
	v_fmac_f32_e32 v22, v12, v13
	v_fmac_f32_e32 v23, v12, v14
	v_lshlrev_b32_e32 v13, 16, v212
	v_and_b32_e32 v14, 0xffff0000, v212
	v_mul_f32_e32 v24, v10, v13
	v_mul_f32_e32 v25, v10, v14
	v_lshlrev_b32_e32 v13, 16, v216
	v_and_b32_e32 v14, 0xffff0000, v216
	v_fmac_f32_e32 v24, v11, v13
	v_fmac_f32_e32 v25, v11, v14
	v_lshlrev_b32_e32 v13, 16, v240
	v_and_b32_e32 v14, 0xffff0000, v240
	v_fmac_f32_e32 v24, v12, v13
	v_fmac_f32_e32 v25, v12, v14
	v_lshlrev_b32_e32 v13, 16, v213
	v_and_b32_e32 v14, 0xffff0000, v213
	v_mul_f32_e32 v26, v10, v13
	v_mul_f32_e32 v27, v10, v14
	v_lshlrev_b32_e32 v13, 16, v217
	v_and_b32_e32 v14, 0xffff0000, v217
	v_fmac_f32_e32 v26, v11, v13
	v_fmac_f32_e32 v27, v11, v14
	v_lshlrev_b32_e32 v13, 16, v241
	v_and_b32_e32 v14, 0xffff0000, v241
	v_fmac_f32_e32 v26, v12, v13
	v_fmac_f32_e32 v27, v12, v14
	v_mov_b32_e32 v16, 0
	v_mov_b32_e32 v17, 0
	v_lshlrev_b32_e32 v7, 3, v209
	v_cvt_pk_fp8_f32 v16, v20, v21
	v_cvt_pk_fp8_f32 v17, v24, v25
	s_nop 0
	v_cvt_pk_fp8_f32 v16, v22, v23 op_sel:[0,0,1]
	v_cvt_pk_fp8_f32 v17, v26, v27 op_sel:[0,0,1]
	s_nop 0
	global_store_dwordx2 v7, v[16:17], s[30:31] sc0 sc1
	s_cmp_le_u32 s44, s43
	s_cbranch_scc1 .Lmg1_loop

.LBB0_339:
	s_ashr_i32 s12, s11, 5
	s_ashr_i32 s13, s12, 31
	s_lshl_b64 s[12:13], s[12:13], 15
	s_add_u32 s12, s2, s12
	s_addc_u32 s13, s3, s13
	v_ashrrev_i32_e32 v25, 31, v24
	v_lshl_add_u64 v[4:5], v[24:25], 2, s[12:13]
	global_store_dword v[4:5], v2, off sc0 sc1

.Lmbm_loop:
	v_add_u32_e32 v238, s46, v2
	v_min_u32_e32 v238, s43, v238
	v_lshrrev_b32_e32 v9, 3, v238
	v_bfe_u32 v8, v238, 15, 5
	v_and_b32_e32 v10, 7, v238
	v_lshlrev_b32_e32 v11, 9, v9
	v_lshlrev_b32_e32 v9, 4, v9
	v_lshl_add_u32 v10, v10, 4, v11
	global_load_dwordx4 v[200:203], v9, s[14:15]
	global_load_dwordx4 v[216:219], v10, s[44:45] offset:384
	v_cmp_lt_u32_e32 vcc, 0, v8
	s_nop 1
	v_cndmask_b32_e32 v11, v150, v148, vcc
	v_add_u32_e32 v11, v11, v10
	global_load_dwordx4 v[204:207], v11, s[44:45]
	v_cmp_lt_u32_e32 vcc, 1, v8
	s_nop 1
	v_cndmask_b32_e32 v11, v150, v64, vcc
	v_add_u32_e32 v11, v11, v10
	global_load_dwordx4 v[208:211], v11, s[44:45]
	v_cmp_lt_u32_e32 vcc, 2, v8
	s_nop 1
	v_cndmask_b32_e32 v11, v150, v65, vcc
	v_add_u32_e32 v11, v11, v10
	global_load_dwordx4 v[212:215], v11, s[44:45]
	v_add_u32_e32 v239, s47, v2
	v_min_u32_e32 v239, s43, v239
	v_lshrrev_b32_e32 v9, 3, v239
	v_bfe_u32 v8, v239, 15, 5
	v_and_b32_e32 v10, 7, v239
	v_lshlrev_b32_e32 v11, 9, v9
	v_lshlrev_b32_e32 v9, 4, v9
	v_lshl_add_u32 v10, v10, 4, v11
	global_load_dwordx4 v[240:243], v9, s[14:15]
	global_load_dwordx4 v[136:139], v10, s[44:45] offset:384
	v_cmp_lt_u32_e32 vcc, 0, v8
	s_nop 1
	v_cndmask_b32_e32 v11, v150, v148, vcc
	v_add_u32_e32 v11, v11, v10
	global_load_dwordx4 v[244:247], v11, s[44:45]
	v_cmp_lt_u32_e32 vcc, 1, v8
	s_nop 1
	v_cndmask_b32_e32 v11, v150, v64, vcc
	v_add_u32_e32 v11, v11, v10
	global_load_dwordx4 v[248:251], v11, s[44:45]
	v_cmp_lt_u32_e32 vcc, 2, v8
	s_nop 1
	v_cndmask_b32_e32 v11, v150, v65, vcc
	v_add_u32_e32 v11, v11, v10
	global_load_dwordx4 v[124:127], v11, s[44:45]
	s_waitcnt vmcnt(10)
	v_bfe_u32 v8, v190, 15, 5
	v_cmp_lt_u32_e32 vcc, 0, v8
	s_nop 1
	v_cndmask_b32_e32 v32, v149, v32, vcc
	v_cmp_lt_u32_e32 vcc, 1, v8
	s_nop 1
	v_cndmask_b32_e32 v33, v149, v33, vcc
	v_cmp_lt_u32_e32 vcc, 2, v8
	s_nop 1
	v_cndmask_b32_e32 v34, v149, v34, vcc
	v_max3_f32 v9, v32, v33, v34
	v_max_f32_e32 v9, v9, v35
	v_sub_f32_e32 v10, v32, v9
	v_mul_f32_e32 v16, 0x3fb8aa3b, v10
	v_fma_f32 v17, v10, s94, -v16
	v_rndne_f32_e32 v18, v16
	v_fmac_f32_e32 v17, 0x32a5705f, v10
	v_sub_f32_e32 v16, v16, v18
	v_add_f32_e32 v16, v16, v17
	v_exp_f32_e32 v12, v16
	v_cvt_i32_f32_e32 v18, v18
	v_cmp_ngt_f32_e32 vcc, s95, v10
	v_ldexp_f32 v12, v12, v18
	s_nop 1
	v_cndmask_b32_e32 v12, 0, v12, vcc
	v_cmp_nlt_f32_e32 vcc, s96, v10
	s_nop 1
	v_cndmask_b32_e32 v12, v227, v12, vcc
	v_sub_f32_e32 v10, v33, v9
	v_mul_f32_e32 v16, 0x3fb8aa3b, v10
	v_fma_f32 v17, v10, s94, -v16
	v_rndne_f32_e32 v18, v16
	v_fmac_f32_e32 v17, 0x32a5705f, v10
	v_sub_f32_e32 v16, v16, v18
	v_add_f32_e32 v16, v16, v17
	v_exp_f32_e32 v13, v16
	v_cvt_i32_f32_e32 v18, v18
	v_cmp_ngt_f32_e32 vcc, s95, v10
	v_ldexp_f32 v13, v13, v18
	s_nop 1
	v_cndmask_b32_e32 v13, 0, v13, vcc
	v_cmp_nlt_f32_e32 vcc, s96, v10
	s_nop 1
	v_cndmask_b32_e32 v13, v227, v13, vcc
	v_sub_f32_e32 v10, v34, v9
	v_mul_f32_e32 v16, 0x3fb8aa3b, v10
	v_fma_f32 v17, v10, s94, -v16
	v_rndne_f32_e32 v18, v16
	v_fmac_f32_e32 v17, 0x32a5705f, v10
	v_sub_f32_e32 v16, v16, v18
	v_add_f32_e32 v16, v16, v17
	v_exp_f32_e32 v14, v16
	v_cvt_i32_f32_e32 v18, v18
	v_cmp_ngt_f32_e32 vcc, s95, v10
	v_ldexp_f32 v14, v14, v18
	s_nop 1
	v_cndmask_b32_e32 v14, 0, v14, vcc
	v_cmp_nlt_f32_e32 vcc, s96, v10
	s_nop 1
	v_cndmask_b32_e32 v14, v227, v14, vcc
	v_sub_f32_e32 v10, v35, v9
	v_mul_f32_e32 v16, 0x3fb8aa3b, v10
	v_fma_f32 v17, v10, s94, -v16
	v_rndne_f32_e32 v18, v16
	v_fmac_f32_e32 v17, 0x32a5705f, v10
	v_sub_f32_e32 v16, v16, v18
	v_add_f32_e32 v16, v16, v17
	v_exp_f32_e32 v15, v16
	v_cvt_i32_f32_e32 v18, v18
	v_cmp_ngt_f32_e32 vcc, s95, v10
	v_ldexp_f32 v15, v15, v18
	s_nop 1
	v_cndmask_b32_e32 v15, 0, v15, vcc
	v_cmp_nlt_f32_e32 vcc, s96, v10
	s_nop 1
	v_cndmask_b32_e32 v15, v227, v15, vcc
	v_add_f32_e32 v16, v12, v13
	v_add_f32_e32 v16, v14, v16
	v_add_f32_e32 v16, v15, v16
	v_div_scale_f32 v17, s[2:3], v16, v16, 1.0
	v_rcp_f32_e32 v18, v17
	s_nop 0
	v_fma_f32 v19, -v17, v18, 1.0
	v_fmac_f32_e32 v18, v19, v18
	v_div_scale_f32 v20, vcc, 1.0, v16, 1.0
	v_mul_f32_e32 v21, v20, v18
	v_fma_f32 v22, -v17, v21, v20
	v_fmac_f32_e32 v21, v22, v18
	v_fma_f32 v17, -v17, v21, v20
	v_div_fmas_f32 v17, v17, v18, v21
	v_div_fixup_f32 v16, v17, v16, 1.0
	v_mul_f32_e32 v16, 0x41800000, v16
	v_mul_f32_e32 v12, v12, v16
	v_mul_f32_e32 v13, v13, v16
	v_mul_f32_e32 v14, v14, v16
	v_mul_f32_e32 v15, v15, v16
	v_lshlrev_b32_e32 v16, 16, v36
	v_and_b32_e32 v17, 0xffff0000, v36
	v_mul_f32_e32 v20, v12, v16
	v_mul_f32_e32 v21, v12, v17
	v_lshlrev_b32_e32 v16, 16, v40
	v_and_b32_e32 v17, 0xffff0000, v40
	v_fmac_f32_e32 v20, v13, v16
	v_fmac_f32_e32 v21, v13, v17
	v_lshlrev_b32_e32 v16, 16, v44
	v_and_b32_e32 v17, 0xffff0000, v44
	v_fmac_f32_e32 v20, v14, v16
	v_fmac_f32_e32 v21, v14, v17
	v_lshlrev_b32_e32 v16, 16, v48
	v_and_b32_e32 v17, 0xffff0000, v48
	v_fmac_f32_e32 v20, v15, v16
	v_fmac_f32_e32 v21, v15, v17
	v_lshlrev_b32_e32 v16, 16, v37
	v_and_b32_e32 v17, 0xffff0000, v37
	v_mul_f32_e32 v22, v12, v16
	v_mul_f32_e32 v23, v12, v17
	v_lshlrev_b32_e32 v16, 16, v41
	v_and_b32_e32 v17, 0xffff0000, v41
	v_fmac_f32_e32 v22, v13, v16
	v_fmac_f32_e32 v23, v13, v17
	v_lshlrev_b32_e32 v16, 16, v45
	v_and_b32_e32 v17, 0xffff0000, v45
	v_fmac_f32_e32 v22, v14, v16
	v_fmac_f32_e32 v23, v14, v17
	v_lshlrev_b32_e32 v16, 16, v49
	v_and_b32_e32 v17, 0xffff0000, v49
	v_fmac_f32_e32 v22, v15, v16
	v_fmac_f32_e32 v23, v15, v17
	v_lshlrev_b32_e32 v16, 16, v38
	v_and_b32_e32 v17, 0xffff0000, v38
	v_mul_f32_e32 v24, v12, v16
	v_mul_f32_e32 v25, v12, v17
	v_lshlrev_b32_e32 v16, 16, v42
	v_and_b32_e32 v17, 0xffff0000, v42
	v_fmac_f32_e32 v24, v13, v16
	v_fmac_f32_e32 v25, v13, v17
	v_lshlrev_b32_e32 v16, 16, v46
	v_and_b32_e32 v17, 0xffff0000, v46
	v_fmac_f32_e32 v24, v14, v16
	v_fmac_f32_e32 v25, v14, v17
	v_lshlrev_b32_e32 v16, 16, v50
	v_and_b32_e32 v17, 0xffff0000, v50
	v_fmac_f32_e32 v24, v15, v16
	v_fmac_f32_e32 v25, v15, v17
	v_lshlrev_b32_e32 v16, 16, v39
	v_and_b32_e32 v17, 0xffff0000, v39
	v_mul_f32_e32 v26, v12, v16
	v_mul_f32_e32 v27, v12, v17
	v_lshlrev_b32_e32 v16, 16, v43
	v_and_b32_e32 v17, 0xffff0000, v43
	v_fmac_f32_e32 v26, v13, v16
	v_fmac_f32_e32 v27, v13, v17
	v_lshlrev_b32_e32 v16, 16, v47
	v_and_b32_e32 v17, 0xffff0000, v47
	v_fmac_f32_e32 v26, v14, v16
	v_fmac_f32_e32 v27, v14, v17
	v_lshlrev_b32_e32 v16, 16, v51
	v_and_b32_e32 v17, 0xffff0000, v51
	v_fmac_f32_e32 v26, v15, v16
	v_fmac_f32_e32 v27, v15, v17
	v_mov_b32_e32 v18, 0
	v_mov_b32_e32 v19, 0
	v_lshlrev_b32_e32 v11, 3, v190
	v_cvt_pk_fp8_f32 v18, v20, v21
	v_cvt_pk_fp8_f32 v19, v24, v25
	s_nop 0
	v_cvt_pk_fp8_f32 v18, v22, v23 op_sel:[0,0,1]
	v_cvt_pk_fp8_f32 v19, v26, v27 op_sel:[0,0,1]
	s_nop 0
	global_store_dwordx2 v11, v[18:19], s[16:17] sc0 sc1
	v_bfe_u32 v8, v191, 15, 5
	v_cmp_lt_u32_e32 vcc, 0, v8
	s_nop 1
	v_cndmask_b32_e32 v52, v149, v52, vcc
	v_cmp_lt_u32_e32 vcc, 1, v8
	s_nop 1
	v_cndmask_b32_e32 v53, v149, v53, vcc
	v_cmp_lt_u32_e32 vcc, 2, v8
	s_nop 1
	v_cndmask_b32_e32 v54, v149, v54, vcc
	v_max3_f32 v9, v52, v53, v54
	v_max_f32_e32 v9, v9, v55
	v_sub_f32_e32 v10, v52, v9
	v_mul_f32_e32 v16, 0x3fb8aa3b, v10
	v_fma_f32 v17, v10, s94, -v16
	v_rndne_f32_e32 v18, v16
	v_fmac_f32_e32 v17, 0x32a5705f, v10
	v_sub_f32_e32 v16, v16, v18
	v_add_f32_e32 v16, v16, v17
	v_exp_f32_e32 v12, v16
	v_cvt_i32_f32_e32 v18, v18
	v_cmp_ngt_f32_e32 vcc, s95, v10
	v_ldexp_f32 v12, v12, v18
	s_nop 1
	v_cndmask_b32_e32 v12, 0, v12, vcc
	v_cmp_nlt_f32_e32 vcc, s96, v10
	s_nop 1
	v_cndmask_b32_e32 v12, v227, v12, vcc
	v_sub_f32_e32 v10, v53, v9
	v_mul_f32_e32 v16, 0x3fb8aa3b, v10
	v_fma_f32 v17, v10, s94, -v16
	v_rndne_f32_e32 v18, v16
	v_fmac_f32_e32 v17, 0x32a5705f, v10
	v_sub_f32_e32 v16, v16, v18
	v_add_f32_e32 v16, v16, v17
	v_exp_f32_e32 v13, v16
	v_cvt_i32_f32_e32 v18, v18
	v_cmp_ngt_f32_e32 vcc, s95, v10
	v_ldexp_f32 v13, v13, v18
	s_nop 1
	v_cndmask_b32_e32 v13, 0, v13, vcc
	v_cmp_nlt_f32_e32 vcc, s96, v10
	s_nop 1
	v_cndmask_b32_e32 v13, v227, v13, vcc
	v_sub_f32_e32 v10, v54, v9
	v_mul_f32_e32 v16, 0x3fb8aa3b, v10
	v_fma_f32 v17, v10, s94, -v16
	v_rndne_f32_e32 v18, v16
	v_fmac_f32_e32 v17, 0x32a5705f, v10
	v_sub_f32_e32 v16, v16, v18
	v_add_f32_e32 v16, v16, v17
	v_exp_f32_e32 v14, v16
	v_cvt_i32_f32_e32 v18, v18
	v_cmp_ngt_f32_e32 vcc, s95, v10
	v_ldexp_f32 v14, v14, v18
	s_nop 1
	v_cndmask_b32_e32 v14, 0, v14, vcc
	v_cmp_nlt_f32_e32 vcc, s96, v10
	s_nop 1
	v_cndmask_b32_e32 v14, v227, v14, vcc
	v_sub_f32_e32 v10, v55, v9
	v_mul_f32_e32 v16, 0x3fb8aa3b, v10
	v_fma_f32 v17, v10, s94, -v16
	v_rndne_f32_e32 v18, v16
	v_fmac_f32_e32 v17, 0x32a5705f, v10
	v_sub_f32_e32 v16, v16, v18
	v_add_f32_e32 v16, v16, v17
	v_exp_f32_e32 v15, v16
	v_cvt_i32_f32_e32 v18, v18
	v_cmp_ngt_f32_e32 vcc, s95, v10
	v_ldexp_f32 v15, v15, v18
	s_nop 1
	v_cndmask_b32_e32 v15, 0, v15, vcc
	v_cmp_nlt_f32_e32 vcc, s96, v10
	s_nop 1
	v_cndmask_b32_e32 v15, v227, v15, vcc
	v_add_f32_e32 v16, v12, v13
	v_add_f32_e32 v16, v14, v16
	v_add_f32_e32 v16, v15, v16
	v_div_scale_f32 v17, s[2:3], v16, v16, 1.0
	v_rcp_f32_e32 v18, v17
	s_nop 0
	v_fma_f32 v19, -v17, v18, 1.0
	v_fmac_f32_e32 v18, v19, v18
	v_div_scale_f32 v20, vcc, 1.0, v16, 1.0
	v_mul_f32_e32 v21, v20, v18
	v_fma_f32 v22, -v17, v21, v20
	v_fmac_f32_e32 v21, v22, v18
	v_fma_f32 v17, -v17, v21, v20
	v_div_fmas_f32 v17, v17, v18, v21
	v_div_fixup_f32 v16, v17, v16, 1.0
	v_mul_f32_e32 v16, 0x41800000, v16
	v_mul_f32_e32 v12, v12, v16
	v_mul_f32_e32 v13, v13, v16
	v_mul_f32_e32 v14, v14, v16
	v_mul_f32_e32 v15, v15, v16
	v_lshlrev_b32_e32 v16, 16, v56
	v_and_b32_e32 v17, 0xffff0000, v56
	v_mul_f32_e32 v20, v12, v16
	v_mul_f32_e32 v21, v12, v17
	v_lshlrev_b32_e32 v16, 16, v60
	v_and_b32_e32 v17, 0xffff0000, v60
	v_fmac_f32_e32 v20, v13, v16
	v_fmac_f32_e32 v21, v13, v17
	v_lshlrev_b32_e32 v16, 16, v192
	v_and_b32_e32 v17, 0xffff0000, v192
	v_fmac_f32_e32 v20, v14, v16
	v_fmac_f32_e32 v21, v14, v17
	v_lshlrev_b32_e32 v16, 16, v196
	v_and_b32_e32 v17, 0xffff0000, v196
	v_fmac_f32_e32 v20, v15, v16
	v_fmac_f32_e32 v21, v15, v17
	v_lshlrev_b32_e32 v16, 16, v57
	v_and_b32_e32 v17, 0xffff0000, v57
	v_mul_f32_e32 v22, v12, v16
	v_mul_f32_e32 v23, v12, v17
	v_lshlrev_b32_e32 v16, 16, v61
	v_and_b32_e32 v17, 0xffff0000, v61
	v_fmac_f32_e32 v22, v13, v16
	v_fmac_f32_e32 v23, v13, v17
	v_lshlrev_b32_e32 v16, 16, v193
	v_and_b32_e32 v17, 0xffff0000, v193
	v_fmac_f32_e32 v22, v14, v16
	v_fmac_f32_e32 v23, v14, v17
	v_lshlrev_b32_e32 v16, 16, v197
	v_and_b32_e32 v17, 0xffff0000, v197
	v_fmac_f32_e32 v22, v15, v16
	v_fmac_f32_e32 v23, v15, v17
	v_lshlrev_b32_e32 v16, 16, v58
	v_and_b32_e32 v17, 0xffff0000, v58
	v_mul_f32_e32 v24, v12, v16
	v_mul_f32_e32 v25, v12, v17
	v_lshlrev_b32_e32 v16, 16, v62
	v_and_b32_e32 v17, 0xffff0000, v62
	v_fmac_f32_e32 v24, v13, v16
	v_fmac_f32_e32 v25, v13, v17
	v_lshlrev_b32_e32 v16, 16, v194
	v_and_b32_e32 v17, 0xffff0000, v194
	v_fmac_f32_e32 v24, v14, v16
	v_fmac_f32_e32 v25, v14, v17
	v_lshlrev_b32_e32 v16, 16, v198
	v_and_b32_e32 v17, 0xffff0000, v198
	v_fmac_f32_e32 v24, v15, v16
	v_fmac_f32_e32 v25, v15, v17
	v_lshlrev_b32_e32 v16, 16, v59
	v_and_b32_e32 v17, 0xffff0000, v59
	v_mul_f32_e32 v26, v12, v16
	v_mul_f32_e32 v27, v12, v17
	v_lshlrev_b32_e32 v16, 16, v63
	v_and_b32_e32 v17, 0xffff0000, v63
	v_fmac_f32_e32 v26, v13, v16
	v_fmac_f32_e32 v27, v13, v17
	v_lshlrev_b32_e32 v16, 16, v195
	v_and_b32_e32 v17, 0xffff0000, v195
	v_fmac_f32_e32 v26, v14, v16
	v_fmac_f32_e32 v27, v14, v17
	v_lshlrev_b32_e32 v16, 16, v199
	v_and_b32_e32 v17, 0xffff0000, v199
	v_fmac_f32_e32 v26, v15, v16
	v_fmac_f32_e32 v27, v15, v17
	v_mov_b32_e32 v18, 0
	v_mov_b32_e32 v19, 0
	v_lshlrev_b32_e32 v11, 3, v191
	v_cvt_pk_fp8_f32 v18, v20, v21
	v_cvt_pk_fp8_f32 v19, v24, v25
	s_nop 0
	v_cvt_pk_fp8_f32 v18, v22, v23 op_sel:[0,0,1]
	v_cvt_pk_fp8_f32 v19, v26, v27 op_sel:[0,0,1]
	s_nop 0
	global_store_dwordx2 v11, v[18:19], s[16:17] sc0 sc1
	v_add_u32_e32 v2, s48, v2
	s_add_u32 s49, s49, s48
	v_min_u32_e32 v190, s43, v2
	v_lshrrev_b32_e32 v9, 3, v190
	v_bfe_u32 v8, v190, 15, 5
	v_and_b32_e32 v10, 7, v190
	v_lshlrev_b32_e32 v11, 9, v9
	v_lshlrev_b32_e32 v9, 4, v9
	v_lshl_add_u32 v10, v10, 4, v11
	global_load_dwordx4 v[32:35], v9, s[14:15]
	global_load_dwordx4 v[48:51], v10, s[44:45] offset:384
	v_cmp_lt_u32_e32 vcc, 0, v8
	s_nop 1
	v_cndmask_b32_e32 v11, v150, v148, vcc
	v_add_u32_e32 v11, v11, v10
	global_load_dwordx4 v[36:39], v11, s[44:45]
	v_cmp_lt_u32_e32 vcc, 1, v8
	s_nop 1
	v_cndmask_b32_e32 v11, v150, v64, vcc
	v_add_u32_e32 v11, v11, v10
	global_load_dwordx4 v[40:43], v11, s[44:45]
	v_cmp_lt_u32_e32 vcc, 2, v8
	s_nop 1
	v_cndmask_b32_e32 v11, v150, v65, vcc
	v_add_u32_e32 v11, v11, v10
	global_load_dwordx4 v[44:47], v11, s[44:45]
	v_add_u32_e32 v191, s42, v2
	v_min_u32_e32 v191, s43, v191
	v_lshrrev_b32_e32 v9, 3, v191
	v_bfe_u32 v8, v191, 15, 5
	v_and_b32_e32 v10, 7, v191
	v_lshlrev_b32_e32 v11, 9, v9
	v_lshlrev_b32_e32 v9, 4, v9
	v_lshl_add_u32 v10, v10, 4, v11
	global_load_dwordx4 v[52:55], v9, s[14:15]
	global_load_dwordx4 v[196:199], v10, s[44:45] offset:384
	v_cmp_lt_u32_e32 vcc, 0, v8
	s_nop 1
	v_cndmask_b32_e32 v11, v150, v148, vcc
	v_add_u32_e32 v11, v11, v10
	global_load_dwordx4 v[56:59], v11, s[44:45]
	v_cmp_lt_u32_e32 vcc, 1, v8
	s_nop 1
	v_cndmask_b32_e32 v11, v150, v64, vcc
	v_add_u32_e32 v11, v11, v10
	global_load_dwordx4 v[60:63], v11, s[44:45]
	v_cmp_lt_u32_e32 vcc, 2, v8
	s_nop 1
	v_cndmask_b32_e32 v11, v150, v65, vcc
	v_add_u32_e32 v11, v11, v10
	global_load_dwordx4 v[192:195], v11, s[44:45]
	s_waitcnt vmcnt(10)
	v_bfe_u32 v8, v238, 15, 5
	v_cmp_lt_u32_e32 vcc, 0, v8
	s_nop 1
	v_cndmask_b32_e32 v200, v149, v200, vcc
	v_cmp_lt_u32_e32 vcc, 1, v8
	s_nop 1
	v_cndmask_b32_e32 v201, v149, v201, vcc
	v_cmp_lt_u32_e32 vcc, 2, v8
	s_nop 1
	v_cndmask_b32_e32 v202, v149, v202, vcc
	v_max3_f32 v9, v200, v201, v202
	v_max_f32_e32 v9, v9, v203
	v_sub_f32_e32 v10, v200, v9
	v_mul_f32_e32 v16, 0x3fb8aa3b, v10
	v_fma_f32 v17, v10, s94, -v16
	v_rndne_f32_e32 v18, v16
	v_fmac_f32_e32 v17, 0x32a5705f, v10
	v_sub_f32_e32 v16, v16, v18
	v_add_f32_e32 v16, v16, v17
	v_exp_f32_e32 v12, v16
	v_cvt_i32_f32_e32 v18, v18
	v_cmp_ngt_f32_e32 vcc, s95, v10
	v_ldexp_f32 v12, v12, v18
	s_nop 1
	v_cndmask_b32_e32 v12, 0, v12, vcc
	v_cmp_nlt_f32_e32 vcc, s96, v10
	s_nop 1
	v_cndmask_b32_e32 v12, v227, v12, vcc
	v_sub_f32_e32 v10, v201, v9
	v_mul_f32_e32 v16, 0x3fb8aa3b, v10
	v_fma_f32 v17, v10, s94, -v16
	v_rndne_f32_e32 v18, v16
	v_fmac_f32_e32 v17, 0x32a5705f, v10
	v_sub_f32_e32 v16, v16, v18
	v_add_f32_e32 v16, v16, v17
	v_exp_f32_e32 v13, v16
	v_cvt_i32_f32_e32 v18, v18
	v_cmp_ngt_f32_e32 vcc, s95, v10
	v_ldexp_f32 v13, v13, v18
	s_nop 1
	v_cndmask_b32_e32 v13, 0, v13, vcc
	v_cmp_nlt_f32_e32 vcc, s96, v10
	s_nop 1
	v_cndmask_b32_e32 v13, v227, v13, vcc
	v_sub_f32_e32 v10, v202, v9
	v_mul_f32_e32 v16, 0x3fb8aa3b, v10
	v_fma_f32 v17, v10, s94, -v16
	v_rndne_f32_e32 v18, v16
	v_fmac_f32_e32 v17, 0x32a5705f, v10
	v_sub_f32_e32 v16, v16, v18
	v_add_f32_e32 v16, v16, v17
	v_exp_f32_e32 v14, v16
	v_cvt_i32_f32_e32 v18, v18
	v_cmp_ngt_f32_e32 vcc, s95, v10
	v_ldexp_f32 v14, v14, v18
	s_nop 1
	v_cndmask_b32_e32 v14, 0, v14, vcc
	v_cmp_nlt_f32_e32 vcc, s96, v10
	s_nop 1
	v_cndmask_b32_e32 v14, v227, v14, vcc
	v_sub_f32_e32 v10, v203, v9
	v_mul_f32_e32 v16, 0x3fb8aa3b, v10
	v_fma_f32 v17, v10, s94, -v16
	v_rndne_f32_e32 v18, v16
	v_fmac_f32_e32 v17, 0x32a5705f, v10
	v_sub_f32_e32 v16, v16, v18
	v_add_f32_e32 v16, v16, v17
	v_exp_f32_e32 v15, v16
	v_cvt_i32_f32_e32 v18, v18
	v_cmp_ngt_f32_e32 vcc, s95, v10
	v_ldexp_f32 v15, v15, v18
	s_nop 1
	v_cndmask_b32_e32 v15, 0, v15, vcc
	v_cmp_nlt_f32_e32 vcc, s96, v10
	s_nop 1
	v_cndmask_b32_e32 v15, v227, v15, vcc
	v_add_f32_e32 v16, v12, v13
	v_add_f32_e32 v16, v14, v16
	v_add_f32_e32 v16, v15, v16
	v_div_scale_f32 v17, s[2:3], v16, v16, 1.0
	v_rcp_f32_e32 v18, v17
	s_nop 0
	v_fma_f32 v19, -v17, v18, 1.0
	v_fmac_f32_e32 v18, v19, v18
	v_div_scale_f32 v20, vcc, 1.0, v16, 1.0
	v_mul_f32_e32 v21, v20, v18
	v_fma_f32 v22, -v17, v21, v20
	v_fmac_f32_e32 v21, v22, v18
	v_fma_f32 v17, -v17, v21, v20
	v_div_fmas_f32 v17, v17, v18, v21
	v_div_fixup_f32 v16, v17, v16, 1.0
	v_mul_f32_e32 v16, 0x41800000, v16
	v_mul_f32_e32 v12, v12, v16
	v_mul_f32_e32 v13, v13, v16
	v_mul_f32_e32 v14, v14, v16
	v_mul_f32_e32 v15, v15, v16
	v_lshlrev_b32_e32 v16, 16, v204
	v_and_b32_e32 v17, 0xffff0000, v204
	v_mul_f32_e32 v20, v12, v16
	v_mul_f32_e32 v21, v12, v17
	v_lshlrev_b32_e32 v16, 16, v208
	v_and_b32_e32 v17, 0xffff0000, v208
	v_fmac_f32_e32 v20, v13, v16
	v_fmac_f32_e32 v21, v13, v17
	v_lshlrev_b32_e32 v16, 16, v212
	v_and_b32_e32 v17, 0xffff0000, v212
	v_fmac_f32_e32 v20, v14, v16
	v_fmac_f32_e32 v21, v14, v17
	v_lshlrev_b32_e32 v16, 16, v216
	v_and_b32_e32 v17, 0xffff0000, v216
	v_fmac_f32_e32 v20, v15, v16
	v_fmac_f32_e32 v21, v15, v17
	v_lshlrev_b32_e32 v16, 16, v205
	v_and_b32_e32 v17, 0xffff0000, v205
	v_mul_f32_e32 v22, v12, v16
	v_mul_f32_e32 v23, v12, v17
	v_lshlrev_b32_e32 v16, 16, v209
	v_and_b32_e32 v17, 0xffff0000, v209
	v_fmac_f32_e32 v22, v13, v16
	v_fmac_f32_e32 v23, v13, v17
	v_lshlrev_b32_e32 v16, 16, v213
	v_and_b32_e32 v17, 0xffff0000, v213
	v_fmac_f32_e32 v22, v14, v16
	v_fmac_f32_e32 v23, v14, v17
	v_lshlrev_b32_e32 v16, 16, v217
	v_and_b32_e32 v17, 0xffff0000, v217
	v_fmac_f32_e32 v22, v15, v16
	v_fmac_f32_e32 v23, v15, v17
	v_lshlrev_b32_e32 v16, 16, v206
	v_and_b32_e32 v17, 0xffff0000, v206
	v_mul_f32_e32 v24, v12, v16
	v_mul_f32_e32 v25, v12, v17
	v_lshlrev_b32_e32 v16, 16, v210
	v_and_b32_e32 v17, 0xffff0000, v210
	v_fmac_f32_e32 v24, v13, v16
	v_fmac_f32_e32 v25, v13, v17
	v_lshlrev_b32_e32 v16, 16, v214
	v_and_b32_e32 v17, 0xffff0000, v214
	v_fmac_f32_e32 v24, v14, v16
	v_fmac_f32_e32 v25, v14, v17
	v_lshlrev_b32_e32 v16, 16, v218
	v_and_b32_e32 v17, 0xffff0000, v218
	v_fmac_f32_e32 v24, v15, v16
	v_fmac_f32_e32 v25, v15, v17
	v_lshlrev_b32_e32 v16, 16, v207
	v_and_b32_e32 v17, 0xffff0000, v207
	v_mul_f32_e32 v26, v12, v16
	v_mul_f32_e32 v27, v12, v17
	v_lshlrev_b32_e32 v16, 16, v211
	v_and_b32_e32 v17, 0xffff0000, v211
	v_fmac_f32_e32 v26, v13, v16
	v_fmac_f32_e32 v27, v13, v17
	v_lshlrev_b32_e32 v16, 16, v215
	v_and_b32_e32 v17, 0xffff0000, v215
	v_fmac_f32_e32 v26, v14, v16
	v_fmac_f32_e32 v27, v14, v17
	v_lshlrev_b32_e32 v16, 16, v219
	v_and_b32_e32 v17, 0xffff0000, v219
	v_fmac_f32_e32 v26, v15, v16
	v_fmac_f32_e32 v27, v15, v17
	v_mov_b32_e32 v18, 0
	v_mov_b32_e32 v19, 0
	v_lshlrev_b32_e32 v11, 3, v238
	v_cvt_pk_fp8_f32 v18, v20, v21
	v_cvt_pk_fp8_f32 v19, v24, v25
	s_nop 0
	v_cvt_pk_fp8_f32 v18, v22, v23 op_sel:[0,0,1]
	v_cvt_pk_fp8_f32 v19, v26, v27 op_sel:[0,0,1]
	s_nop 0
	global_store_dwordx2 v11, v[18:19], s[16:17] sc0 sc1
	v_bfe_u32 v8, v239, 15, 5
	v_cmp_lt_u32_e32 vcc, 0, v8
	s_nop 1
	v_cndmask_b32_e32 v240, v149, v240, vcc
	v_cmp_lt_u32_e32 vcc, 1, v8
	s_nop 1
	v_cndmask_b32_e32 v241, v149, v241, vcc
	v_cmp_lt_u32_e32 vcc, 2, v8
	s_nop 1
	v_cndmask_b32_e32 v242, v149, v242, vcc
	v_max3_f32 v9, v240, v241, v242
	v_max_f32_e32 v9, v9, v243
	v_sub_f32_e32 v10, v240, v9
	v_mul_f32_e32 v16, 0x3fb8aa3b, v10
	v_fma_f32 v17, v10, s94, -v16
	v_rndne_f32_e32 v18, v16
	v_fmac_f32_e32 v17, 0x32a5705f, v10
	v_sub_f32_e32 v16, v16, v18
	v_add_f32_e32 v16, v16, v17
	v_exp_f32_e32 v12, v16
	v_cvt_i32_f32_e32 v18, v18
	v_cmp_ngt_f32_e32 vcc, s95, v10
	v_ldexp_f32 v12, v12, v18
	s_nop 1
	v_cndmask_b32_e32 v12, 0, v12, vcc
	v_cmp_nlt_f32_e32 vcc, s96, v10
	s_nop 1
	v_cndmask_b32_e32 v12, v227, v12, vcc
	v_sub_f32_e32 v10, v241, v9
	v_mul_f32_e32 v16, 0x3fb8aa3b, v10
	v_fma_f32 v17, v10, s94, -v16
	v_rndne_f32_e32 v18, v16
	v_fmac_f32_e32 v17, 0x32a5705f, v10
	v_sub_f32_e32 v16, v16, v18
	v_add_f32_e32 v16, v16, v17
	v_exp_f32_e32 v13, v16
	v_cvt_i32_f32_e32 v18, v18
	v_cmp_ngt_f32_e32 vcc, s95, v10
	v_ldexp_f32 v13, v13, v18
	s_nop 1
	v_cndmask_b32_e32 v13, 0, v13, vcc
	v_cmp_nlt_f32_e32 vcc, s96, v10
	s_nop 1
	v_cndmask_b32_e32 v13, v227, v13, vcc
	v_sub_f32_e32 v10, v242, v9
	v_mul_f32_e32 v16, 0x3fb8aa3b, v10
	v_fma_f32 v17, v10, s94, -v16
	v_rndne_f32_e32 v18, v16
	v_fmac_f32_e32 v17, 0x32a5705f, v10
	v_sub_f32_e32 v16, v16, v18
	v_add_f32_e32 v16, v16, v17
	v_exp_f32_e32 v14, v16
	v_cvt_i32_f32_e32 v18, v18
	v_cmp_ngt_f32_e32 vcc, s95, v10
	v_ldexp_f32 v14, v14, v18
	s_nop 1
	v_cndmask_b32_e32 v14, 0, v14, vcc
	v_cmp_nlt_f32_e32 vcc, s96, v10
	s_nop 1
	v_cndmask_b32_e32 v14, v227, v14, vcc
	v_sub_f32_e32 v10, v243, v9
	v_mul_f32_e32 v16, 0x3fb8aa3b, v10
	v_fma_f32 v17, v10, s94, -v16
	v_rndne_f32_e32 v18, v16
	v_fmac_f32_e32 v17, 0x32a5705f, v10
	v_sub_f32_e32 v16, v16, v18
	v_add_f32_e32 v16, v16, v17
	v_exp_f32_e32 v15, v16
	v_cvt_i32_f32_e32 v18, v18
	v_cmp_ngt_f32_e32 vcc, s95, v10
	v_ldexp_f32 v15, v15, v18
	s_nop 1
	v_cndmask_b32_e32 v15, 0, v15, vcc
	v_cmp_nlt_f32_e32 vcc, s96, v10
	s_nop 1
	v_cndmask_b32_e32 v15, v227, v15, vcc
	v_add_f32_e32 v16, v12, v13
	v_add_f32_e32 v16, v14, v16
	v_add_f32_e32 v16, v15, v16
	v_div_scale_f32 v17, s[2:3], v16, v16, 1.0
	v_rcp_f32_e32 v18, v17
	s_nop 0
	v_fma_f32 v19, -v17, v18, 1.0
	v_fmac_f32_e32 v18, v19, v18
	v_div_scale_f32 v20, vcc, 1.0, v16, 1.0
	v_mul_f32_e32 v21, v20, v18
	v_fma_f32 v22, -v17, v21, v20
	v_fmac_f32_e32 v21, v22, v18
	v_fma_f32 v17, -v17, v21, v20
	v_div_fmas_f32 v17, v17, v18, v21
	v_div_fixup_f32 v16, v17, v16, 1.0
	v_mul_f32_e32 v16, 0x41800000, v16
	v_mul_f32_e32 v12, v12, v16
	v_mul_f32_e32 v13, v13, v16
	v_mul_f32_e32 v14, v14, v16
	v_mul_f32_e32 v15, v15, v16
	v_lshlrev_b32_e32 v16, 16, v244
	v_and_b32_e32 v17, 0xffff0000, v244
	v_mul_f32_e32 v20, v12, v16
	v_mul_f32_e32 v21, v12, v17
	v_lshlrev_b32_e32 v16, 16, v248
	v_and_b32_e32 v17, 0xffff0000, v248
	v_fmac_f32_e32 v20, v13, v16
	v_fmac_f32_e32 v21, v13, v17
	v_lshlrev_b32_e32 v16, 16, v124
	v_and_b32_e32 v17, 0xffff0000, v124
	v_fmac_f32_e32 v20, v14, v16
	v_fmac_f32_e32 v21, v14, v17
	v_lshlrev_b32_e32 v16, 16, v136
	v_and_b32_e32 v17, 0xffff0000, v136
	v_fmac_f32_e32 v20, v15, v16
	v_fmac_f32_e32 v21, v15, v17
	v_lshlrev_b32_e32 v16, 16, v245
	v_and_b32_e32 v17, 0xffff0000, v245
	v_mul_f32_e32 v22, v12, v16
	v_mul_f32_e32 v23, v12, v17
	v_lshlrev_b32_e32 v16, 16, v249
	v_and_b32_e32 v17, 0xffff0000, v249
	v_fmac_f32_e32 v22, v13, v16
	v_fmac_f32_e32 v23, v13, v17
	v_lshlrev_b32_e32 v16, 16, v125
	v_and_b32_e32 v17, 0xffff0000, v125
	v_fmac_f32_e32 v22, v14, v16
	v_fmac_f32_e32 v23, v14, v17
	v_lshlrev_b32_e32 v16, 16, v137
	v_and_b32_e32 v17, 0xffff0000, v137
	v_fmac_f32_e32 v22, v15, v16
	v_fmac_f32_e32 v23, v15, v17
	v_lshlrev_b32_e32 v16, 16, v246
	v_and_b32_e32 v17, 0xffff0000, v246
	v_mul_f32_e32 v24, v12, v16
	v_mul_f32_e32 v25, v12, v17
	v_lshlrev_b32_e32 v16, 16, v250
	v_and_b32_e32 v17, 0xffff0000, v250
	v_fmac_f32_e32 v24, v13, v16
	v_fmac_f32_e32 v25, v13, v17
	v_lshlrev_b32_e32 v16, 16, v126
	v_and_b32_e32 v17, 0xffff0000, v126
	v_fmac_f32_e32 v24, v14, v16
	v_fmac_f32_e32 v25, v14, v17
	v_lshlrev_b32_e32 v16, 16, v138
	v_and_b32_e32 v17, 0xffff0000, v138
	v_fmac_f32_e32 v24, v15, v16
	v_fmac_f32_e32 v25, v15, v17
	v_lshlrev_b32_e32 v16, 16, v247
	v_and_b32_e32 v17, 0xffff0000, v247
	v_mul_f32_e32 v26, v12, v16
	v_mul_f32_e32 v27, v12, v17
	v_lshlrev_b32_e32 v16, 16, v251
	v_and_b32_e32 v17, 0xffff0000, v251
	v_fmac_f32_e32 v26, v13, v16
	v_fmac_f32_e32 v27, v13, v17
	v_lshlrev_b32_e32 v16, 16, v127
	v_and_b32_e32 v17, 0xffff0000, v127
	v_fmac_f32_e32 v26, v14, v16
	v_fmac_f32_e32 v27, v14, v17
	v_lshlrev_b32_e32 v16, 16, v139
	v_and_b32_e32 v17, 0xffff0000, v139
	v_fmac_f32_e32 v26, v15, v16
	v_fmac_f32_e32 v27, v15, v17
	v_mov_b32_e32 v18, 0
	v_mov_b32_e32 v19, 0
	v_lshlrev_b32_e32 v11, 3, v239
	v_cvt_pk_fp8_f32 v18, v20, v21
	v_cvt_pk_fp8_f32 v19, v24, v25
	s_nop 0
	v_cvt_pk_fp8_f32 v18, v22, v23 op_sel:[0,0,1]
	v_cvt_pk_fp8_f32 v19, v26, v27 op_sel:[0,0,1]
	s_nop 0
	global_store_dwordx2 v11, v[18:19], s[16:17] sc0 sc1
	s_cmp_le_u32 s49, s43
	s_cbranch_scc1 .Lmbm_loop

.LBB0_1302:
	s_or_b64 exec, exec, s[0:1]
	s_add_i32 s0, s29, 0xfffffdbf
	v_lshl_add_u32 v2, v2, 2, 0
	v_mov_b32_e32 v235, v231
	s_cmp_lt_u32 s0, 0xffffffc0
	s_waitcnt vmcnt(0)
	ds_write_b32 v2, v0 offset:57344
	s_waitcnt lgkmcnt(0)
	s_barrier
	s_cselect_b64 s[0:1], -1, 0
	v_and_b32_e32 v234, 31, v235
	s_or_b64 s[42:43], s[68:69], s[0:1]
	v_and_b32_e32 v233, 32, v235
	v_and_b32_e32 v0, 7, v235
	v_mul_u32_u24_e32 v2, 0x48, v234
	s_mov_b64 s[0:1], -1
	s_and_b64 vcc, exec, s[42:43]
	v_lshlrev_b32_e32 v237, 4, v0
	v_or_b32_e32 v236, s28, v0
	v_add_lshl_u32 v232, v2, v233, 1
	s_cbranch_vccnz .LBB0_1320
	v_lshrrev_b32_e32 v0, 2, v235
	v_readlane_b32 s0, v255, 5
	v_mov_b32_e32 v240, v232
	v_readlane_b32 s1, v255, 9
	v_and_or_b32 v0, v0, 14, s0
	s_movk_i32 s0, 0x48
	v_mul_lo_u32 v2, v236, s0
	v_lshl_or_b32 v238, v0, 10, v237
	v_add_lshl_u32 v239, v2, v0, 1
	v_lshlrev_b32_e32 v0, 2, v234
	v_readlane_b32 s0, v255, 7
	s_mov_b64 s[42:43], s[36:37]
	v_add_u32_e32 v244, 0, v239
	v_add_u32_e32 v2, s0, v0
	v_add_u32_e32 v2, 0xd800, v2
	ds_read2_b32 v[2:3], v2 offset1:32
	s_mov_b32 s0, 0x24000
	v_add_u32_e32 v0, s1, v0
	s_cmp_lt_i32 s83, s29
	v_add_u32_e32 v245, 0, v240
	s_waitcnt lgkmcnt(0)
	v_lshlrev_b32_e32 v4, 7, v2
	v_and_b32_e32 v4, 0xfffffc00, v4
	v_cmp_ne_u32_e32 vcc, s0, v2
	s_mov_b32 s2, 0
	v_add_u32_e32 v246, s33, v245
	v_cndmask_b32_e32 v2, 0, v4, vcc
	v_or_b32_e32 v241, v2, v233
	v_lshlrev_b32_e32 v2, 7, v3
	v_and_b32_e32 v2, 0xfffffc00, v2
	v_cmp_ne_u32_e32 vcc, s0, v3
	s_movk_i32 s49, 0x80
	s_mov_b32 s39, 0
	v_cndmask_b32_e32 v2, 0, v2, vcc
	v_or_b32_e32 v242, v2, v233
	global_load_dwordx4 v[204:207], v241, s[54:55] offset:16
	global_load_dwordx4 v[212:215], v241, s[54:55]
	global_load_dwordx4 v[192:195], v242, s[54:55] offset:16
	global_load_dwordx4 v[208:211], v242, s[54:55]
	ds_read_b32 v0, v0 offset:57344
	s_waitcnt lgkmcnt(0)
	v_lshlrev_b32_e32 v2, 7, v0
	v_and_b32_e32 v2, 0xfffffc00, v2
	v_cmp_ne_u32_e32 vcc, s0, v0
	s_mov_b64 s[0:1], s[34:35]
	s_nop 0
	v_cndmask_b32_e32 v0, 0, v2, vcc
	v_or_b32_e32 v243, v0, v233
	v_mov_b32_e32 v0, v238
	global_load_dwordx4 v[200:203], v243, s[54:55] offset:16
	global_load_dwordx4 v[196:199], v243, s[54:55]
	global_load_dwordx4 v[2:5], v0, s[0:1] nt
	global_load_dwordx4 v[6:9], v0, s[0:1] offset:1024 nt
	global_load_dwordx4 v[10:13], v0, s[42:43] nt
	global_load_dwordx4 v[14:17], v0, s[42:43] offset:1024 nt
	s_mov_b64 s[0:1], s[92:93]
	s_mov_b64 s[42:43], s[96:97]
	v_mov_b32_e32 v0, v238
	global_load_dwordx4 v[160:163], v0, s[42:43] nt
	global_load_dwordx4 v[164:167], v0, s[42:43] offset:1024 nt
	global_load_dwordx4 v[168:171], v0, s[0:1] nt
	global_load_dwordx4 v[172:175], v0, s[0:1] offset:1024 nt
	s_mov_b64 s[42:43], s[88:89]
	s_mov_b64 s[0:1], s[8:9]
	s_waitcnt vmcnt(6)
	v_cvt_pk_bf16_f32 v0, v2, v6
	v_mov_b32_e32 v6, v1
	s_waitcnt vmcnt(4)
	v_cvt_pk_bf16_f32 v2, v10, v14
	ds_write2_b32 v244, v0, v2 offset1:8
	v_cvt_pk_bf16_f32 v0, v3, v7
	v_cvt_pk_bf16_f32 v2, v11, v15
	v_add_u32_e32 v3, 0x400, v244
	ds_write2_b32 v3, v0, v2 offset0:32 offset1:40
	v_cvt_pk_bf16_f32 v0, v4, v8
	v_cvt_pk_bf16_f32 v2, v12, v16
	v_add_u32_e32 v3, 0x800, v244
	ds_write2_b32 v3, v0, v2 offset0:64 offset1:72
	v_cvt_pk_bf16_f32 v0, v5, v9
	v_cvt_pk_bf16_f32 v2, v13, v17
	v_add_u32_e32 v3, 0xc00, v244
	ds_write2_b32 v3, v0, v2 offset0:96 offset1:104
	v_mov_b32_e32 v0, v238
	global_load_dwordx4 v[176:179], v0, s[42:43] nt
	global_load_dwordx4 v[180:183], v0, s[42:43] offset:1024 nt
	global_load_dwordx4 v[184:187], v0, s[0:1] nt
	global_load_dwordx4 v[188:191], v0, s[0:1] offset:1024 nt
	v_mov_b32_e32 v14, v1
	v_mov_b32_e32 v15, v1
	s_cselect_b64 s[0:1], -1, 0
	v_mov_b32_e32 v0, v1
	v_mov_b32_e32 v2, v1
	v_mov_b32_e32 v3, v1
	v_mov_b32_e32 v4, v1
	v_mov_b32_e32 v5, v1
	v_mov_b32_e32 v7, v1
	v_mov_b32_e32 v8, v1
	v_mov_b32_e32 v9, v1
	v_mov_b32_e32 v10, v1
	v_mov_b32_e32 v11, v1
	v_mov_b32_e32 v12, v1
	v_mov_b32_e32 v13, v1
	v_mov_b32_e32 v16, 0
	s_cmp_lt_i32 s80, s29
	v_mov_b64_e32 v[46:47], v[14:15]
	v_mov_b64_e32 v[78:79], v[14:15]
	v_mov_b64_e32 v[62:63], v[14:15]
	v_mov_b64_e32 v[94:95], v[14:15]
	v_mov_b64_e32 v[110:111], v[14:15]
	v_mov_b64_e32 v[142:143], v[14:15]
	v_mov_b64_e32 v[126:127], v[14:15]
	v_mov_b64_e32 v[158:159], v[14:15]
	s_cselect_b64 s[44:45], -1, 0
	v_mov_b64_e32 v[44:45], v[12:13]
	v_mov_b64_e32 v[42:43], v[10:11]
	v_mov_b64_e32 v[40:41], v[8:9]
	v_mov_b64_e32 v[38:39], v[6:7]
	v_mov_b64_e32 v[36:37], v[4:5]
	v_mov_b64_e32 v[34:35], v[2:3]
	v_mov_b64_e32 v[32:33], v[0:1]
	v_mov_b64_e32 v[76:77], v[12:13]
	v_mov_b64_e32 v[74:75], v[10:11]
	v_mov_b64_e32 v[72:73], v[8:9]
	v_mov_b64_e32 v[70:71], v[6:7]
	v_mov_b64_e32 v[68:69], v[4:5]
	v_mov_b64_e32 v[66:67], v[2:3]
	v_mov_b64_e32 v[64:65], v[0:1]
	v_mov_b64_e32 v[60:61], v[12:13]
	v_mov_b64_e32 v[58:59], v[10:11]
	v_mov_b64_e32 v[56:57], v[8:9]
	v_mov_b64_e32 v[54:55], v[6:7]
	v_mov_b64_e32 v[52:53], v[4:5]
	v_mov_b64_e32 v[50:51], v[2:3]
	v_mov_b64_e32 v[48:49], v[0:1]
	v_mov_b64_e32 v[92:93], v[12:13]
	v_mov_b64_e32 v[90:91], v[10:11]
	v_mov_b64_e32 v[88:89], v[8:9]
	v_mov_b64_e32 v[86:87], v[6:7]
	v_mov_b64_e32 v[84:85], v[4:5]
	v_mov_b64_e32 v[82:83], v[2:3]
	v_mov_b64_e32 v[80:81], v[0:1]
	v_mov_b64_e32 v[108:109], v[12:13]
	v_mov_b64_e32 v[106:107], v[10:11]
	v_mov_b64_e32 v[104:105], v[8:9]
	v_mov_b64_e32 v[102:103], v[6:7]
	v_mov_b64_e32 v[100:101], v[4:5]
	v_mov_b64_e32 v[98:99], v[2:3]
	v_mov_b64_e32 v[96:97], v[0:1]
	v_mov_b64_e32 v[140:141], v[12:13]
	v_mov_b64_e32 v[138:139], v[10:11]
	v_mov_b64_e32 v[136:137], v[8:9]
	v_mov_b64_e32 v[134:135], v[6:7]
	v_mov_b64_e32 v[132:133], v[4:5]
	v_mov_b64_e32 v[130:131], v[2:3]
	v_mov_b64_e32 v[128:129], v[0:1]
	v_mov_b64_e32 v[124:125], v[12:13]
	v_mov_b64_e32 v[122:123], v[10:11]
	v_mov_b64_e32 v[120:121], v[8:9]
	v_mov_b64_e32 v[118:119], v[6:7]
	v_mov_b64_e32 v[116:117], v[4:5]
	v_mov_b64_e32 v[114:115], v[2:3]
	v_mov_b64_e32 v[112:113], v[0:1]
	v_mov_b64_e32 v[156:157], v[12:13]
	v_mov_b64_e32 v[154:155], v[10:11]
	v_mov_b64_e32 v[152:153], v[8:9]
	v_mov_b64_e32 v[150:151], v[6:7]
	v_mov_b64_e32 v[148:149], v[4:5]
	v_mov_b64_e32 v[146:147], v[2:3]
	v_mov_b64_e32 v[144:145], v[0:1]
	v_mov_b32_e32 v17, v16
	v_mov_b32_e32 v18, v16
	v_mov_b32_e32 v19, v16
	v_mov_b32_e32 v20, v16
	v_mov_b32_e32 v21, v16
	v_mov_b32_e32 v22, v16
	v_mov_b32_e32 v23, v16
	v_mov_b32_e32 v24, v16
	v_mov_b32_e32 v25, v16
	v_mov_b32_e32 v26, v16
	v_mov_b32_e32 v27, v16
	v_mov_b32_e32 v28, v16
	v_mov_b32_e32 v29, v16
	v_mov_b32_e32 v30, v16
	v_mov_b32_e32 v31, v16
	s_branch .LBB0_1306

.LBB0_1306:
	s_add_i32 s25, s2, 1
	s_cmp_lg_u32 s2, 2
	s_cselect_b32 s26, s25, 0
	s_mul_i32 s25, s26, 0x4800
	s_add_i32 s56, s25, 0
	s_add_i32 s25, s39, 3
	s_cmp_lt_u32 s39, 61
	s_cselect_b32 s25, s25, 0
	s_lshr_b32 s42, s25, 4
	s_add_i32 s42, s42, s66
	s_and_b32 s42, s42, 3
	s_add_i32 s42, s42, s27
	s_lshl_b32 s25, s25, 16
	s_lshl_b32 s42, s42, 8
	s_and_b32 s25, s25, 0xf0000
	v_add_u32_e32 v0, s56, v239
	s_waitcnt vmcnt(6)
	v_cvt_pk_bf16_f32 v2, v160, v164
	s_waitcnt vmcnt(4)
	v_cvt_pk_bf16_f32 v3, v168, v172
	s_or_b32 s25, s42, s25
	s_waitcnt lgkmcnt(0)
	s_barrier
	ds_write2_b32 v0, v2, v3 offset1:8
	v_cvt_pk_bf16_f32 v2, v161, v165
	v_cvt_pk_bf16_f32 v3, v169, v173
	v_add_u32_e32 v4, 0x400, v0
	s_add_u32 s42, s67, s25
	ds_write2_b32 v4, v2, v3 offset0:32 offset1:40
	v_cvt_pk_bf16_f32 v2, v162, v166
	v_cvt_pk_bf16_f32 v3, v170, v174
	v_add_u32_e32 v4, 0x800, v0
	s_addc_u32 s43, s38, 0
	ds_write2_b32 v4, v2, v3 offset0:64 offset1:72
	v_cvt_pk_bf16_f32 v2, v163, v167
	v_cvt_pk_bf16_f32 v3, v171, v175
	v_add_u32_e32 v0, 0xc00, v0
	s_add_u32 s46, s42, 0x4000
	ds_write2_b32 v0, v2, v3 offset0:96 offset1:104
	s_addc_u32 s47, s43, 0
	v_mov_b32_e32 v0, v238
	global_load_dwordx4 v[160:163], v0, s[42:43] nt
	global_load_dwordx4 v[164:167], v0, s[42:43] offset:1024 nt
	global_load_dwordx4 v[168:171], v0, s[46:47] nt
	global_load_dwordx4 v[172:175], v0, s[46:47] offset:1024 nt
	s_add_i32 s25, s49, 0xffffff80
	s_and_b32 s25, s25, 0x380
	s_or_b32 s25, s25, 64
	s_add_u32 s46, s25, s54
	v_cndmask_b32_e64 v0, 0, 1, s[0:1]
	s_addc_u32 s47, 0, s55
	s_mul_i32 s90, s2, 0x4800
	v_cmp_ne_u32_e64 s[42:43], 1, v0
	s_andn2_b64 vcc, exec, s[0:1]
	s_cbranch_vccnz .LBB0_1308
	v_cvt_pk_f32_fp8_e32 v[6:7], v212
	v_cvt_pk_f32_fp8_sdwa v[8:9], v212 src0_sel:WORD_1
	v_cvt_pk_f32_fp8_e32 v[10:11], v213
	v_cvt_pk_f32_fp8_sdwa v[12:13], v213 src0_sel:WORD_1
	v_add_u32_e32 v0, s90, v245
	ds_read_b128 v[2:5], v0
	v_cvt_pk_bf16_f32 v6, v6, v7
	v_cvt_pk_bf16_f32 v7, v8, v9
	v_cvt_pk_bf16_f32 v8, v10, v11
	v_cvt_pk_bf16_f32 v9, v12, v13
	ds_read_b128 v[10:13], v0 offset:4608
	ds_read_b128 v[248:251], v0 offset:9216
	ds_read_b128 v[216:219], v0 offset:13824
	s_waitcnt lgkmcnt(3)
	v_mfma_f32_32x32x16_bf16 v[144:159], v[2:5], v[6:9], v[144:159]
	s_waitcnt vmcnt(6)
	v_cvt_pk_f32_fp8_e32 v[14:15], v209
	s_waitcnt lgkmcnt(2)
	v_mfma_f32_32x32x16_bf16 v[112:127], v[10:13], v[6:9], v[112:127]
	s_waitcnt lgkmcnt(1)
	v_mfma_f32_32x32x16_bf16 v[128:143], v[248:251], v[6:9], v[128:143]
	s_waitcnt lgkmcnt(0)
	v_mfma_f32_32x32x16_bf16 v[96:111], v[216:219], v[6:9], v[96:111]
	v_cvt_pk_f32_fp8_e32 v[6:7], v208
	v_cvt_pk_f32_fp8_sdwa v[8:9], v208 src0_sel:WORD_1
	v_cvt_pk_f32_fp8_sdwa v[208:209], v209 src0_sel:WORD_1
	v_cvt_pk_bf16_f32 v6, v6, v7
	v_cvt_pk_bf16_f32 v7, v8, v9
	v_cvt_pk_bf16_f32 v8, v14, v15
	v_cvt_pk_bf16_f32 v9, v208, v209
	v_cvt_pk_f32_fp8_e32 v[14:15], v211
	v_cvt_pk_f32_fp8_sdwa v[208:209], v211 src0_sel:WORD_1
	v_mfma_f32_32x32x16_bf16 v[80:95], v[2:5], v[6:9], v[80:95]
	ds_read_b128 v[2:5], v0 offset:16
	v_mfma_f32_32x32x16_bf16 v[48:63], v[10:13], v[6:9], v[48:63]
	v_cvt_pk_f32_fp8_e32 v[10:11], v215
	v_cvt_pk_f32_fp8_sdwa v[12:13], v215 src0_sel:WORD_1
	v_mfma_f32_32x32x16_bf16 v[64:79], v[248:251], v[6:9], v[64:79]
	v_mfma_f32_32x32x16_bf16 v[32:47], v[216:219], v[6:9], v[32:47]
	v_cvt_pk_f32_fp8_e32 v[6:7], v214
	v_cvt_pk_f32_fp8_sdwa v[8:9], v214 src0_sel:WORD_1
	ds_read_b128 v[212:215], v0 offset:9232
	ds_read_b128 v[216:219], v0 offset:13840
	v_cvt_pk_bf16_f32 v6, v6, v7
	v_cvt_pk_bf16_f32 v7, v8, v9
	v_cvt_pk_bf16_f32 v8, v10, v11
	v_cvt_pk_bf16_f32 v9, v12, v13
	ds_read_b128 v[10:13], v0 offset:4624
	s_waitcnt lgkmcnt(3)
	v_mfma_f32_32x32x16_bf16 v[144:159], v[2:5], v[6:9], v[144:159]
	s_waitcnt lgkmcnt(0)
	v_mfma_f32_32x32x16_bf16 v[112:127], v[10:13], v[6:9], v[112:127]
	v_mfma_f32_32x32x16_bf16 v[128:143], v[212:215], v[6:9], v[128:143]
	v_mfma_f32_32x32x16_bf16 v[96:111], v[216:219], v[6:9], v[96:111]
	v_cvt_pk_f32_fp8_e32 v[6:7], v210
	v_cvt_pk_f32_fp8_sdwa v[8:9], v210 src0_sel:WORD_1
	v_cvt_pk_bf16_f32 v6, v6, v7
	v_cvt_pk_bf16_f32 v7, v8, v9
	v_cvt_pk_bf16_f32 v8, v14, v15
	v_cvt_pk_bf16_f32 v9, v208, v209
	ds_read_b128 v[208:211], v0 offset:9248
	v_cvt_pk_f32_fp8_e32 v[14:15], v193
	v_mfma_f32_32x32x16_bf16 v[80:95], v[2:5], v[6:9], v[80:95]
	ds_read_b128 v[2:5], v0 offset:32
	v_mfma_f32_32x32x16_bf16 v[48:63], v[10:13], v[6:9], v[48:63]
	v_cvt_pk_f32_fp8_e32 v[10:11], v205
	v_cvt_pk_f32_fp8_sdwa v[12:13], v205 src0_sel:WORD_1
	v_mfma_f32_32x32x16_bf16 v[64:79], v[212:215], v[6:9], v[64:79]
	ds_read_b128 v[212:215], v0 offset:13856
	v_mfma_f32_32x32x16_bf16 v[32:47], v[216:219], v[6:9], v[32:47]
	v_cvt_pk_f32_fp8_e32 v[6:7], v204
	v_cvt_pk_f32_fp8_sdwa v[8:9], v204 src0_sel:WORD_1
	v_cvt_pk_bf16_f32 v6, v6, v7
	v_cvt_pk_bf16_f32 v7, v8, v9
	v_cvt_pk_bf16_f32 v8, v10, v11
	v_cvt_pk_bf16_f32 v9, v12, v13
	ds_read_b128 v[10:13], v0 offset:4640
	s_waitcnt lgkmcnt(2)
	v_mfma_f32_32x32x16_bf16 v[144:159], v[2:5], v[6:9], v[144:159]
	s_waitcnt lgkmcnt(0)
	v_mfma_f32_32x32x16_bf16 v[112:127], v[10:13], v[6:9], v[112:127]
	v_mfma_f32_32x32x16_bf16 v[128:143], v[208:211], v[6:9], v[128:143]
	v_mfma_f32_32x32x16_bf16 v[96:111], v[212:215], v[6:9], v[96:111]
	v_cvt_pk_f32_fp8_e32 v[6:7], v192
	v_cvt_pk_f32_fp8_sdwa v[8:9], v192 src0_sel:WORD_1
	v_cvt_pk_f32_fp8_sdwa v[192:193], v193 src0_sel:WORD_1
	v_cvt_pk_bf16_f32 v6, v6, v7
	v_cvt_pk_bf16_f32 v7, v8, v9
	v_cvt_pk_bf16_f32 v8, v14, v15
	v_cvt_pk_bf16_f32 v9, v192, v193
	v_cvt_pk_f32_fp8_e32 v[14:15], v195
	v_cvt_pk_f32_fp8_sdwa v[192:193], v195 src0_sel:WORD_1
	v_mfma_f32_32x32x16_bf16 v[80:95], v[2:5], v[6:9], v[80:95]
	ds_read_b128 v[2:5], v0 offset:48
	v_mfma_f32_32x32x16_bf16 v[48:63], v[10:13], v[6:9], v[48:63]
	v_cvt_pk_f32_fp8_e32 v[10:11], v207
	v_cvt_pk_f32_fp8_sdwa v[12:13], v207 src0_sel:WORD_1
	v_mfma_f32_32x32x16_bf16 v[64:79], v[208:211], v[6:9], v[64:79]
	ds_read_b128 v[208:211], v0 offset:13872
	v_mfma_f32_32x32x16_bf16 v[32:47], v[212:215], v[6:9], v[32:47]
	v_cvt_pk_f32_fp8_e32 v[6:7], v206
	v_cvt_pk_f32_fp8_sdwa v[8:9], v206 src0_sel:WORD_1
	ds_read_b128 v[204:207], v0 offset:9264
	v_cvt_pk_bf16_f32 v6, v6, v7
	v_cvt_pk_bf16_f32 v7, v8, v9
	v_cvt_pk_bf16_f32 v8, v10, v11
	v_cvt_pk_bf16_f32 v9, v12, v13
	ds_read_b128 v[10:13], v0 offset:4656
	s_waitcnt lgkmcnt(3)
	v_mfma_f32_32x32x16_bf16 v[144:159], v[2:5], v[6:9], v[144:159]
	s_waitcnt lgkmcnt(0)
	v_mfma_f32_32x32x16_bf16 v[112:127], v[10:13], v[6:9], v[112:127]
	v_mfma_f32_32x32x16_bf16 v[128:143], v[204:207], v[6:9], v[128:143]
	v_mfma_f32_32x32x16_bf16 v[96:111], v[208:211], v[6:9], v[96:111]
	v_cvt_pk_f32_fp8_e32 v[6:7], v194
	v_cvt_pk_f32_fp8_sdwa v[8:9], v194 src0_sel:WORD_1
	v_cvt_pk_bf16_f32 v6, v6, v7
	v_cvt_pk_bf16_f32 v7, v8, v9
	v_cvt_pk_bf16_f32 v8, v14, v15
	v_cvt_pk_bf16_f32 v9, v192, v193
	s_nop 1
	v_mfma_f32_32x32x16_bf16 v[80:95], v[2:5], v[6:9], v[80:95]
	v_mfma_f32_32x32x16_bf16 v[48:63], v[10:13], v[6:9], v[48:63]
	v_mfma_f32_32x32x16_bf16 v[64:79], v[204:207], v[6:9], v[64:79]
	v_mfma_f32_32x32x16_bf16 v[32:47], v[208:211], v[6:9], v[32:47]
.LBB0_1308:
	v_mov_b32_e32 v0, v241
	s_waitcnt vmcnt(5)
	v_cvt_pk_f32_fp8_e32 v[2:3], v196
	v_cvt_pk_f32_fp8_sdwa v[4:5], v196 src0_sel:WORD_1
	v_cvt_pk_f32_fp8_e32 v[10:11], v197
	v_cvt_pk_f32_fp8_sdwa v[12:13], v197 src0_sel:WORD_1
	global_load_dwordx4 v[192:195], v0, s[46:47] offset:16
	global_load_dwordx4 v[208:211], v0, s[46:47]
	v_mov_b32_e32 v0, v242
	global_load_dwordx4 v[6:9], v0, s[46:47] offset:16
	global_load_dwordx4 v[204:207], v0, s[46:47]
	v_add_u32_e32 v0, s90, v246
	v_cvt_pk_bf16_f32 v2, v2, v3
	v_cvt_pk_bf16_f32 v3, v4, v5
	v_cvt_pk_bf16_f32 v4, v10, v11
	v_cvt_pk_bf16_f32 v5, v12, v13
	ds_read_b128 v[10:13], v0
	v_cvt_pk_f32_fp8_sdwa v[14:15], v199 src0_sel:WORD_1
	s_waitcnt lgkmcnt(0)
	v_mfma_f32_32x32x16_bf16 v[16:31], v[10:13], v[2:5], v[16:31]
	v_cvt_pk_f32_fp8_e32 v[2:3], v198
	v_cvt_pk_f32_fp8_sdwa v[4:5], v198 src0_sel:WORD_1
	v_cvt_pk_f32_fp8_e32 v[12:13], v199
	s_add_i32 s2, s26, 1
	v_cvt_pk_bf16_f32 v10, v2, v3
	v_mov_b32_e32 v2, v243
	v_cvt_pk_bf16_f32 v11, v4, v5
	global_load_dwordx4 v[2:5], v2, s[46:47]
	ds_read_b128 v[196:199], v0 offset:16
	ds_read_b128 v[212:215], v0 offset:32
	v_cvt_pk_bf16_f32 v12, v12, v13
	v_cvt_pk_bf16_f32 v13, v14, v15
	s_waitcnt vmcnt(9)
	v_cvt_pk_f32_fp8_e32 v[14:15], v201
	s_cmp_lg_u32 s26, 2
	s_waitcnt lgkmcnt(1)
	v_mfma_f32_32x32x16_bf16 v[16:31], v[196:199], v[10:13], v[16:31]
	v_cvt_pk_f32_fp8_e32 v[10:11], v200
	v_cvt_pk_f32_fp8_sdwa v[12:13], v200 src0_sel:WORD_1
	v_cvt_pk_f32_fp8_sdwa v[196:197], v201 src0_sel:WORD_1
	v_cvt_pk_f32_fp8_sdwa v[200:201], v203 src0_sel:WORD_1
	v_cvt_pk_bf16_f32 v10, v10, v11
	v_cvt_pk_bf16_f32 v11, v12, v13
	v_cvt_pk_bf16_f32 v12, v14, v15
	v_cvt_pk_bf16_f32 v13, v196, v197
	s_cselect_b32 s2, s2, 0
	s_mul_i32 s25, s2, 0x4800
	s_waitcnt lgkmcnt(0)
	v_mfma_f32_32x32x16_bf16 v[16:31], v[212:215], v[10:13], v[16:31]
	v_cvt_pk_f32_fp8_e32 v[10:11], v202
	v_cvt_pk_f32_fp8_sdwa v[12:13], v202 src0_sel:WORD_1
	v_cvt_pk_f32_fp8_e32 v[14:15], v203
	v_cvt_pk_bf16_f32 v199, v200, v201
	v_cvt_pk_bf16_f32 v196, v10, v11
	v_mov_b32_e32 v10, v243
	ds_read_b128 v[200:203], v0 offset:48
	v_add_u32_e32 v0, s25, v244
	s_add_i32 s25, s39, 4
	s_cmp_lt_u32 s39, 60
	s_cselect_b32 s25, s25, 0
	s_lshr_b32 s26, s25, 4
	s_add_i32 s26, s26, s66
	s_and_b32 s26, s26, 3
	s_add_i32 s26, s26, s27
	s_lshl_b32 s25, s25, 16
	s_lshl_b32 s26, s26, 8
	s_and_b32 s25, s25, 0xe0000
	v_cvt_pk_bf16_f32 v198, v14, v15
	s_waitcnt vmcnt(11)
	v_cvt_pk_bf16_f32 v14, v176, v180
	s_waitcnt vmcnt(9)
	v_cvt_pk_bf16_f32 v15, v184, v188
	s_or_b32 s25, s26, s25
	v_cvt_pk_bf16_f32 v197, v12, v13
	global_load_dwordx4 v[10:13], v10, s[46:47] offset:16
	s_waitcnt lgkmcnt(0)
	s_barrier
	ds_write2_b32 v0, v14, v15 offset1:8
	v_cvt_pk_bf16_f32 v14, v177, v181
	v_cvt_pk_bf16_f32 v15, v185, v189
	v_add_u32_e32 v176, 0x400, v0
	s_add_u32 s46, s67, s25
	ds_write2_b32 v176, v14, v15 offset0:32 offset1:40
	v_cvt_pk_bf16_f32 v14, v178, v182
	v_cvt_pk_bf16_f32 v15, v186, v190
	v_add_u32_e32 v176, 0x800, v0
	s_addc_u32 s47, s38, 0
	ds_write2_b32 v176, v14, v15 offset0:64 offset1:72
	v_cvt_pk_bf16_f32 v14, v179, v183
	v_cvt_pk_bf16_f32 v15, v187, v191
	v_add_u32_e32 v0, 0xc00, v0
	s_add_u32 s90, s46, 0x4000
	ds_write2_b32 v0, v14, v15 offset0:96 offset1:104
	s_addc_u32 s91, s47, 0
	v_mov_b32_e32 v0, v238
	global_load_dwordx4 v[176:179], v0, s[46:47] nt
	global_load_dwordx4 v[180:183], v0, s[46:47] offset:1024 nt
	global_load_dwordx4 v[184:187], v0, s[90:91] nt
	global_load_dwordx4 v[188:191], v0, s[90:91] offset:1024 nt
	v_mfma_f32_32x32x16_bf16 v[16:31], v[200:203], v[196:199], v[16:31]
	s_cmp_gt_u32 s39, 61
	s_cselect_b64 s[46:47], -1, 0
	s_and_b32 s25, s49, 0x380
	s_cmp_lt_u32 s39, 62
	s_cselect_b32 s25, s25, 0
	s_add_u32 s90, s25, s54
	s_addc_u32 s91, 0, s55
	s_and_b64 vcc, exec, s[42:43]
	s_cbranch_vccnz .LBB0_1310
	s_waitcnt vmcnt(8)
	v_cvt_pk_f32_fp8_sdwa v[202:203], v208 src0_sel:WORD_1
	v_cvt_pk_f32_fp8_e32 v[212:213], v209
	v_add_u32_e32 v0, s56, v240
	ds_read_b128 v[196:199], v0
	v_cvt_pk_bf16_f32 v201, v202, v203
	v_cvt_pk_bf16_f32 v202, v212, v213
	ds_read_b128 v[212:215], v0 offset:4608
	ds_read_b128 v[216:219], v0 offset:9216
	ds_read_b128 v[248:251], v0 offset:13824
	v_cvt_pk_f32_fp8_e32 v[14:15], v208
	v_cvt_pk_f32_fp8_sdwa v[208:209], v209 src0_sel:WORD_1
	v_cvt_pk_bf16_f32 v200, v14, v15
	v_cvt_pk_bf16_f32 v203, v208, v209
	s_waitcnt vmcnt(6)
	v_cvt_pk_f32_fp8_e32 v[14:15], v204
	v_cvt_pk_f32_fp8_e32 v[208:209], v205
	s_waitcnt lgkmcnt(3)
	v_mfma_f32_32x32x16_bf16 v[144:159], v[196:199], v[200:203], v[144:159]
	s_waitcnt lgkmcnt(2)
	v_mfma_f32_32x32x16_bf16 v[112:127], v[212:215], v[200:203], v[112:127]
	s_waitcnt lgkmcnt(1)
	v_mfma_f32_32x32x16_bf16 v[128:143], v[216:219], v[200:203], v[128:143]
	s_waitcnt lgkmcnt(0)
	v_mfma_f32_32x32x16_bf16 v[96:111], v[248:251], v[200:203], v[96:111]
	v_cvt_pk_f32_fp8_sdwa v[202:203], v204 src0_sel:WORD_1
	v_cvt_pk_f32_fp8_sdwa v[204:205], v205 src0_sel:WORD_1
	v_cvt_pk_bf16_f32 v200, v14, v15
	v_cvt_pk_f32_fp8_e32 v[14:15], v210
	v_cvt_pk_bf16_f32 v201, v202, v203
	v_cvt_pk_bf16_f32 v202, v208, v209
	v_cvt_pk_bf16_f32 v203, v204, v205
	v_cvt_pk_f32_fp8_sdwa v[208:209], v211 src0_sel:WORD_1
	v_cvt_pk_f32_fp8_e32 v[204:205], v211
	v_mfma_f32_32x32x16_bf16 v[80:95], v[196:199], v[200:203], v[80:95]
	ds_read_b128 v[196:199], v0 offset:16
	v_mfma_f32_32x32x16_bf16 v[48:63], v[212:215], v[200:203], v[48:63]
	ds_read_b128 v[212:215], v0 offset:9232
	v_mfma_f32_32x32x16_bf16 v[64:79], v[216:219], v[200:203], v[64:79]
	ds_read_b128 v[216:219], v0 offset:13840
	v_mfma_f32_32x32x16_bf16 v[32:47], v[248:251], v[200:203], v[32:47]
	v_cvt_pk_f32_fp8_sdwa v[202:203], v210 src0_sel:WORD_1
	v_cvt_pk_bf16_f32 v200, v14, v15
	v_cvt_pk_f32_fp8_e32 v[14:15], v206
	v_cvt_pk_bf16_f32 v201, v202, v203
	v_cvt_pk_bf16_f32 v203, v208, v209
	ds_read_b128 v[208:211], v0 offset:4624
	v_cvt_pk_bf16_f32 v202, v204, v205
	v_cvt_pk_f32_fp8_e32 v[204:205], v207
	s_waitcnt lgkmcnt(3)
	v_mfma_f32_32x32x16_bf16 v[144:159], v[196:199], v[200:203], v[144:159]
	s_waitcnt lgkmcnt(0)
	v_mfma_f32_32x32x16_bf16 v[112:127], v[208:211], v[200:203], v[112:127]
	v_mfma_f32_32x32x16_bf16 v[128:143], v[212:215], v[200:203], v[128:143]
	v_mfma_f32_32x32x16_bf16 v[96:111], v[216:219], v[200:203], v[96:111]
	v_cvt_pk_f32_fp8_sdwa v[202:203], v206 src0_sel:WORD_1
	v_cvt_pk_f32_fp8_sdwa v[206:207], v207 src0_sel:WORD_1
	v_cvt_pk_bf16_f32 v200, v14, v15
	v_cvt_pk_f32_fp8_e32 v[14:15], v192
	v_cvt_pk_bf16_f32 v201, v202, v203
	v_cvt_pk_bf16_f32 v202, v204, v205
	v_cvt_pk_bf16_f32 v203, v206, v207
	v_cvt_pk_f32_fp8_e32 v[204:205], v193
	s_nop 0
	v_mfma_f32_32x32x16_bf16 v[80:95], v[196:199], v[200:203], v[80:95]
	ds_read_b128 v[196:199], v0 offset:32
	v_mfma_f32_32x32x16_bf16 v[48:63], v[208:211], v[200:203], v[48:63]
	ds_read_b128 v[208:211], v0 offset:9248
	v_mfma_f32_32x32x16_bf16 v[64:79], v[212:215], v[200:203], v[64:79]
	ds_read_b128 v[212:215], v0 offset:13856
	v_mfma_f32_32x32x16_bf16 v[32:47], v[216:219], v[200:203], v[32:47]
	v_cvt_pk_f32_fp8_sdwa v[202:203], v192 src0_sel:WORD_1
	v_cvt_pk_f32_fp8_sdwa v[192:193], v193 src0_sel:WORD_1
	v_cvt_pk_bf16_f32 v200, v14, v15
	v_cvt_pk_f32_fp8_e32 v[14:15], v6
	v_cvt_pk_bf16_f32 v201, v202, v203
	v_cvt_pk_bf16_f32 v202, v204, v205
	ds_read_b128 v[204:207], v0 offset:4640
	v_cvt_pk_bf16_f32 v203, v192, v193
	v_cvt_pk_f32_fp8_sdwa v[192:193], v6 src0_sel:WORD_1
	s_waitcnt lgkmcnt(3)
	v_mfma_f32_32x32x16_bf16 v[144:159], v[196:199], v[200:203], v[144:159]
	s_waitcnt lgkmcnt(0)
	v_mfma_f32_32x32x16_bf16 v[112:127], v[204:207], v[200:203], v[112:127]
	v_mfma_f32_32x32x16_bf16 v[128:143], v[208:211], v[200:203], v[128:143]
	v_mfma_f32_32x32x16_bf16 v[96:111], v[212:215], v[200:203], v[96:111]
	v_cvt_pk_f32_fp8_e32 v[202:203], v7
	v_cvt_pk_f32_fp8_sdwa v[6:7], v7 src0_sel:WORD_1
	v_cvt_pk_bf16_f32 v200, v14, v15
	v_cvt_pk_bf16_f32 v201, v192, v193
	v_cvt_pk_bf16_f32 v202, v202, v203
	v_cvt_pk_bf16_f32 v203, v6, v7
	v_cvt_pk_f32_fp8_e32 v[6:7], v194
	v_cvt_pk_f32_fp8_sdwa v[14:15], v194 src0_sel:WORD_1
	v_mfma_f32_32x32x16_bf16 v[80:95], v[196:199], v[200:203], v[80:95]
	ds_read_b128 v[196:199], v0 offset:48
	v_cvt_pk_bf16_f32 v192, v6, v7
	v_cvt_pk_bf16_f32 v193, v14, v15
	v_cvt_pk_f32_fp8_e32 v[6:7], v8
	v_cvt_pk_f32_fp8_sdwa v[14:15], v8 src0_sel:WORD_1
	v_cvt_pk_bf16_f32 v6, v6, v7
	v_mfma_f32_32x32x16_bf16 v[48:63], v[204:207], v[200:203], v[48:63]
	ds_read_b128 v[204:207], v0 offset:9264
	v_cvt_pk_bf16_f32 v7, v14, v15
	v_mfma_f32_32x32x16_bf16 v[64:79], v[208:211], v[200:203], v[64:79]
	ds_read_b128 v[208:211], v0 offset:13872
	v_mfma_f32_32x32x16_bf16 v[32:47], v[212:215], v[200:203], v[32:47]
	v_cvt_pk_f32_fp8_e32 v[200:201], v195
	v_cvt_pk_f32_fp8_sdwa v[202:203], v195 src0_sel:WORD_1
	v_cvt_pk_bf16_f32 v194, v200, v201
	v_cvt_pk_bf16_f32 v195, v202, v203
	ds_read_b128 v[200:203], v0 offset:4656
	s_waitcnt lgkmcnt(3)
	v_mfma_f32_32x32x16_bf16 v[144:159], v[196:199], v[192:195], v[144:159]
	s_waitcnt lgkmcnt(0)
	v_mfma_f32_32x32x16_bf16 v[112:127], v[200:203], v[192:195], v[112:127]
	v_mfma_f32_32x32x16_bf16 v[128:143], v[204:207], v[192:195], v[128:143]
	v_mfma_f32_32x32x16_bf16 v[96:111], v[208:211], v[192:195], v[96:111]
	v_cvt_pk_f32_fp8_e32 v[192:193], v9
	v_cvt_pk_f32_fp8_sdwa v[194:195], v9 src0_sel:WORD_1
	v_cvt_pk_bf16_f32 v8, v192, v193
	v_cvt_pk_bf16_f32 v9, v194, v195
	s_nop 1
	v_mfma_f32_32x32x16_bf16 v[80:95], v[196:199], v[6:9], v[80:95]
	v_mfma_f32_32x32x16_bf16 v[48:63], v[200:203], v[6:9], v[48:63]
	v_mfma_f32_32x32x16_bf16 v[64:79], v[204:207], v[6:9], v[64:79]
	v_mfma_f32_32x32x16_bf16 v[32:47], v[208:211], v[6:9], v[32:47]

.LBB0_1320:
	s_and_b64 vcc, exec, s[0:1]
	s_cbranch_vccz .LBB0_1295
	v_lshrrev_b32_e32 v0, 3, v235
	v_readlane_b32 s0, v255, 3
	s_mov_b64 s[42:43], s[30:31]
	s_min_i32 s2, s29, 0x400
	v_and_or_b32 v0, v0, 7, s0
	s_movk_i32 s0, 0x90
	v_mul_lo_u32 v2, v236, s0
	s_waitcnt vmcnt(3)
	v_lshl_or_b32 v192, v0, 11, v237
	v_lshl_add_u32 v193, v0, 2, v2
	v_lshl_add_u32 v0, v234, 2, s41
	v_add_u32_e32 v0, 0xd800, v0
	ds_read2_b32 v[2:3], v0 offset1:32
	s_mov_b32 s0, 0x24000
	s_waitcnt vmcnt(1)
	v_add_u32_e32 v196, 0, v193
	s_mov_b32 s49, 2
	s_mov_b32 s29, 0
	s_waitcnt lgkmcnt(0)
	v_lshlrev_b32_e32 v0, 7, v2
	v_and_b32_e32 v0, 0xfffffc00, v0
	v_cmp_ne_u32_e32 vcc, s0, v2
	v_add_u32_e32 v197, 0, v232
	s_nop 0
	v_cndmask_b32_e32 v0, 0, v0, vcc
	v_or_b32_e32 v194, v0, v233
	v_lshlrev_b32_e32 v0, 7, v3
	v_and_b32_e32 v0, 0xfffffc00, v0
	v_cmp_ne_u32_e32 vcc, s0, v3
	s_mov_b64 s[0:1], s[94:95]
	s_nop 0
	v_cndmask_b32_e32 v0, 0, v0, vcc
	v_or_b32_e32 v195, v0, v233
	v_mov_b32_e32 v0, v192
	global_load_dwordx4 v[180:183], v194, s[54:55] offset:16
	global_load_dwordx4 v[188:191], v194, s[54:55]
	global_load_dwordx4 v[176:179], v195, s[54:55] offset:16
	global_load_dwordx4 v[184:187], v195, s[54:55]
	global_load_dwordx4 v[2:5], v0, s[42:43] nt
	global_load_dwordx4 v[6:9], v0, s[42:43] offset:1024 nt
	global_load_dwordx4 v[10:13], v0, s[0:1] nt
	global_load_dwordx4 v[14:17], v0, s[0:1] offset:1024 nt
	s_mov_b64 s[0:1], s[12:13]
	s_mov_b64 s[42:43], s[14:15]
	v_mov_b32_e32 v0, v192
	global_load_dwordx4 v[144:147], v0, s[0:1] nt
	global_load_dwordx4 v[148:151], v0, s[0:1] offset:1024 nt
	global_load_dwordx4 v[152:155], v0, s[42:43] nt
	global_load_dwordx4 v[156:159], v0, s[42:43] offset:1024 nt
	s_mov_b64 s[0:1], s[18:19]
	s_mov_b64 s[42:43], s[16:17]
	s_waitcnt vmcnt(6)
	v_cvt_pk_bf16_f32 v0, v2, v6
	v_mov_b32_e32 v6, v1
	s_waitcnt vmcnt(4)
	v_cvt_pk_bf16_f32 v2, v10, v14
	ds_write2_b32 v196, v0, v2 offset1:8
	v_cvt_pk_bf16_f32 v0, v3, v7
	v_cvt_pk_bf16_f32 v2, v11, v15
	v_add_u32_e32 v3, 0x400, v196
	ds_write2_b32 v3, v0, v2 offset0:32 offset1:40
	v_cvt_pk_bf16_f32 v0, v4, v8
	v_cvt_pk_bf16_f32 v2, v12, v16
	v_add_u32_e32 v3, 0x800, v196
	ds_write2_b32 v3, v0, v2 offset0:64 offset1:72
	v_cvt_pk_bf16_f32 v0, v5, v9
	v_cvt_pk_bf16_f32 v2, v13, v17
	v_add_u32_e32 v3, 0xc00, v196
	ds_write2_b32 v3, v0, v2 offset0:96 offset1:104
	v_mov_b32_e32 v0, v192
	global_load_dwordx4 v[160:163], v0, s[42:43] nt
	global_load_dwordx4 v[164:167], v0, s[42:43] offset:1024 nt
	global_load_dwordx4 v[168:171], v0, s[0:1] nt
	global_load_dwordx4 v[172:175], v0, s[0:1] offset:1024 nt
	s_sub_i32 s0, s2, s82
	s_cmp_lt_i32 s83, s0
	v_mov_b32_e32 v14, v1
	v_mov_b32_e32 v15, v1
	s_cselect_b64 s[42:43], -1, 0
	v_mov_b32_e32 v0, v1
	v_mov_b32_e32 v2, v1
	v_mov_b32_e32 v3, v1
	v_mov_b32_e32 v4, v1
	v_mov_b32_e32 v5, v1
	v_mov_b32_e32 v7, v1
	v_mov_b32_e32 v8, v1
	v_mov_b32_e32 v9, v1
	v_mov_b32_e32 v10, v1
	v_mov_b32_e32 v11, v1
	v_mov_b32_e32 v12, v1
	v_mov_b32_e32 v13, v1
	s_cmp_lt_i32 s80, s0
	v_mov_b64_e32 v[30:31], v[14:15]
	v_mov_b64_e32 v[62:63], v[14:15]
	v_mov_b64_e32 v[46:47], v[14:15]
	v_mov_b64_e32 v[78:79], v[14:15]
	v_mov_b64_e32 v[94:95], v[14:15]
	v_mov_b64_e32 v[126:127], v[14:15]
	v_mov_b64_e32 v[110:111], v[14:15]
	v_mov_b64_e32 v[142:143], v[14:15]
	s_movk_i32 s2, 0x80
	s_cselect_b64 s[44:45], -1, 0
	v_mov_b64_e32 v[28:29], v[12:13]
	v_mov_b64_e32 v[26:27], v[10:11]
	v_mov_b64_e32 v[24:25], v[8:9]
	v_mov_b64_e32 v[22:23], v[6:7]
	v_mov_b64_e32 v[20:21], v[4:5]
	v_mov_b64_e32 v[18:19], v[2:3]
	v_mov_b64_e32 v[16:17], v[0:1]
	v_mov_b64_e32 v[60:61], v[12:13]
	v_mov_b64_e32 v[58:59], v[10:11]
	v_mov_b64_e32 v[56:57], v[8:9]
	v_mov_b64_e32 v[54:55], v[6:7]
	v_mov_b64_e32 v[52:53], v[4:5]
	v_mov_b64_e32 v[50:51], v[2:3]
	v_mov_b64_e32 v[48:49], v[0:1]
	v_mov_b64_e32 v[44:45], v[12:13]
	v_mov_b64_e32 v[42:43], v[10:11]
	v_mov_b64_e32 v[40:41], v[8:9]
	v_mov_b64_e32 v[38:39], v[6:7]
	v_mov_b64_e32 v[36:37], v[4:5]
	v_mov_b64_e32 v[34:35], v[2:3]
	v_mov_b64_e32 v[32:33], v[0:1]
	v_mov_b64_e32 v[76:77], v[12:13]
	v_mov_b64_e32 v[74:75], v[10:11]
	v_mov_b64_e32 v[72:73], v[8:9]
	v_mov_b64_e32 v[70:71], v[6:7]
	v_mov_b64_e32 v[68:69], v[4:5]
	v_mov_b64_e32 v[66:67], v[2:3]
	v_mov_b64_e32 v[64:65], v[0:1]
	v_mov_b64_e32 v[92:93], v[12:13]
	v_mov_b64_e32 v[90:91], v[10:11]
	v_mov_b64_e32 v[88:89], v[8:9]
	v_mov_b64_e32 v[86:87], v[6:7]
	v_mov_b64_e32 v[84:85], v[4:5]
	v_mov_b64_e32 v[82:83], v[2:3]
	v_mov_b64_e32 v[80:81], v[0:1]
	v_mov_b64_e32 v[124:125], v[12:13]
	v_mov_b64_e32 v[122:123], v[10:11]
	v_mov_b64_e32 v[120:121], v[8:9]
	v_mov_b64_e32 v[118:119], v[6:7]
	v_mov_b64_e32 v[116:117], v[4:5]
	v_mov_b64_e32 v[114:115], v[2:3]
	v_mov_b64_e32 v[112:113], v[0:1]
	v_mov_b64_e32 v[108:109], v[12:13]
	v_mov_b64_e32 v[106:107], v[10:11]
	v_mov_b64_e32 v[104:105], v[8:9]
	v_mov_b64_e32 v[102:103], v[6:7]
	v_mov_b64_e32 v[100:101], v[4:5]
	v_mov_b64_e32 v[98:99], v[2:3]
	v_mov_b64_e32 v[96:97], v[0:1]
	v_mov_b64_e32 v[140:141], v[12:13]
	v_mov_b64_e32 v[138:139], v[10:11]
	v_mov_b64_e32 v[136:137], v[8:9]
	v_mov_b64_e32 v[134:135], v[6:7]
	v_mov_b64_e32 v[132:133], v[4:5]
	v_mov_b64_e32 v[130:131], v[2:3]
	v_mov_b64_e32 v[128:129], v[0:1]
	s_branch .LBB0_1324

.LBB0_1324:
	s_add_i32 s0, s29, 1
	s_cmp_lg_u32 s29, 2
	s_cselect_b32 s39, s0, 0
	s_mul_i32 s0, s39, 0x4800
	s_add_i32 s26, s0, 0
	s_add_i32 s0, s49, 1
	s_cmp_lt_u32 s0, s40
	s_cselect_b32 s0, s0, 0
	s_lshr_b32 s1, s0, 4
	s_add_i32 s1, s1, s76
	s_and_b32 s1, s1, s77
	s_add_i32 s1, s1, s27
	s_lshl_b32 s0, s0, 14
	s_lshl_b32 s1, s1, 6
	s_and_b32 s0, s0, 0x3c000
	s_add_i32 s56, s1, s0
	v_add_u32_e32 v0, s26, v193
	s_waitcnt vmcnt(6)
	v_cvt_pk_bf16_f32 v2, v144, v148
	s_waitcnt vmcnt(4)
	v_cvt_pk_bf16_f32 v3, v152, v156
	s_lshl_b64 s[0:1], s[56:57], 2
	s_waitcnt lgkmcnt(0)
	s_barrier
	ds_write2_b32 v0, v2, v3 offset1:8
	v_cvt_pk_bf16_f32 v2, v145, v149
	v_cvt_pk_bf16_f32 v3, v153, v157
	v_add_u32_e32 v4, 0x400, v0
	s_add_u32 s0, s11, s0
	ds_write2_b32 v4, v2, v3 offset0:32 offset1:40
	v_cvt_pk_bf16_f32 v2, v146, v150
	v_cvt_pk_bf16_f32 v3, v154, v158
	v_add_u32_e32 v4, 0x800, v0
	s_addc_u32 s1, s79, s1
	ds_write2_b32 v4, v2, v3 offset0:64 offset1:72
	v_cvt_pk_bf16_f32 v2, v147, v151
	v_cvt_pk_bf16_f32 v3, v155, v159
	v_add_u32_e32 v0, 0xc00, v0
	s_add_u32 s46, s0, 0x4000
	ds_write2_b32 v0, v2, v3 offset0:96 offset1:104
	s_addc_u32 s47, s1, 0
	v_mov_b32_e32 v0, v192
	global_load_dwordx4 v[144:147], v0, s[0:1] nt
	global_load_dwordx4 v[148:151], v0, s[0:1] offset:1024 nt
	global_load_dwordx4 v[152:155], v0, s[46:47] nt
	global_load_dwordx4 v[156:159], v0, s[46:47] offset:1024 nt
	s_sub_i32 s1, s2, 64
	s_add_i32 s0, s49, -1
	s_and_b32 s1, s1, 0x3c0
	s_cmp_lt_u32 s0, s40
	s_cselect_b32 s0, s1, 0
	s_add_u32 s46, s0, s54
	v_cndmask_b32_e64 v0, 0, 1, s[42:43]
	s_addc_u32 s47, 0, s55
	v_cmp_ne_u32_e64 s[0:1], 1, v0
	s_andn2_b64 vcc, exec, s[42:43]
	s_cbranch_vccnz .LBB0_1326
	s_waitcnt vmcnt(6)
	v_cvt_pk_f32_fp8_e32 v[6:7], v188
	v_cvt_pk_f32_fp8_sdwa v[8:9], v188 src0_sel:WORD_1
	v_cvt_pk_f32_fp8_e32 v[10:11], v189
	v_cvt_pk_f32_fp8_sdwa v[12:13], v189 src0_sel:WORD_1
	s_mul_i32 s25, s29, 0x4800
	v_add_u32_e32 v0, s25, v197
	ds_read_b128 v[2:5], v0
	v_cvt_pk_bf16_f32 v6, v6, v7
	v_cvt_pk_bf16_f32 v7, v8, v9
	v_cvt_pk_bf16_f32 v8, v10, v11
	v_cvt_pk_bf16_f32 v9, v12, v13
	ds_read_b128 v[10:13], v0 offset:4608
	ds_read_b128 v[198:201], v0 offset:9216
	ds_read_b128 v[202:205], v0 offset:13824
	s_waitcnt lgkmcnt(3)
	v_mfma_f32_32x32x16_bf16 v[128:143], v[2:5], v[6:9], v[128:143]
	s_waitcnt vmcnt(4)
	v_cvt_pk_f32_fp8_e32 v[14:15], v185
	s_waitcnt lgkmcnt(2)
	v_mfma_f32_32x32x16_bf16 v[96:111], v[10:13], v[6:9], v[96:111]
	s_waitcnt lgkmcnt(1)
	v_mfma_f32_32x32x16_bf16 v[112:127], v[198:201], v[6:9], v[112:127]
	s_waitcnt lgkmcnt(0)
	v_mfma_f32_32x32x16_bf16 v[80:95], v[202:205], v[6:9], v[80:95]
	v_cvt_pk_f32_fp8_e32 v[6:7], v184
	v_cvt_pk_f32_fp8_sdwa v[8:9], v184 src0_sel:WORD_1
	v_cvt_pk_f32_fp8_sdwa v[184:185], v185 src0_sel:WORD_1
	v_cvt_pk_bf16_f32 v6, v6, v7
	v_cvt_pk_bf16_f32 v7, v8, v9
	v_cvt_pk_bf16_f32 v8, v14, v15
	v_cvt_pk_bf16_f32 v9, v184, v185
	v_cvt_pk_f32_fp8_e32 v[14:15], v187
	v_cvt_pk_f32_fp8_sdwa v[184:185], v187 src0_sel:WORD_1
	v_mfma_f32_32x32x16_bf16 v[64:79], v[2:5], v[6:9], v[64:79]
	ds_read_b128 v[2:5], v0 offset:16
	v_mfma_f32_32x32x16_bf16 v[32:47], v[10:13], v[6:9], v[32:47]
	v_cvt_pk_f32_fp8_e32 v[10:11], v191
	v_cvt_pk_f32_fp8_sdwa v[12:13], v191 src0_sel:WORD_1
	v_mfma_f32_32x32x16_bf16 v[48:63], v[198:201], v[6:9], v[48:63]
	ds_read_b128 v[198:201], v0 offset:13840
	v_mfma_f32_32x32x16_bf16 v[16:31], v[202:205], v[6:9], v[16:31]
	v_cvt_pk_f32_fp8_e32 v[6:7], v190
	v_cvt_pk_f32_fp8_sdwa v[8:9], v190 src0_sel:WORD_1
	ds_read_b128 v[188:191], v0 offset:9232
	v_cvt_pk_bf16_f32 v6, v6, v7
	v_cvt_pk_bf16_f32 v7, v8, v9
	v_cvt_pk_bf16_f32 v8, v10, v11
	v_cvt_pk_bf16_f32 v9, v12, v13
	ds_read_b128 v[10:13], v0 offset:4624
	s_waitcnt lgkmcnt(3)
	v_mfma_f32_32x32x16_bf16 v[128:143], v[2:5], v[6:9], v[128:143]
	s_waitcnt lgkmcnt(0)
	v_mfma_f32_32x32x16_bf16 v[96:111], v[10:13], v[6:9], v[96:111]
	v_mfma_f32_32x32x16_bf16 v[112:127], v[188:191], v[6:9], v[112:127]
	v_mfma_f32_32x32x16_bf16 v[80:95], v[198:201], v[6:9], v[80:95]
	v_cvt_pk_f32_fp8_e32 v[6:7], v186
	v_cvt_pk_f32_fp8_sdwa v[8:9], v186 src0_sel:WORD_1
	v_cvt_pk_bf16_f32 v6, v6, v7
	v_cvt_pk_bf16_f32 v7, v8, v9
	v_cvt_pk_bf16_f32 v8, v14, v15
	v_cvt_pk_bf16_f32 v9, v184, v185
	ds_read_b128 v[184:187], v0 offset:9248
	v_cvt_pk_f32_fp8_e32 v[14:15], v177
	v_mfma_f32_32x32x16_bf16 v[64:79], v[2:5], v[6:9], v[64:79]
	ds_read_b128 v[2:5], v0 offset:32
	v_mfma_f32_32x32x16_bf16 v[32:47], v[10:13], v[6:9], v[32:47]
	v_cvt_pk_f32_fp8_e32 v[10:11], v181
	v_cvt_pk_f32_fp8_sdwa v[12:13], v181 src0_sel:WORD_1
	v_mfma_f32_32x32x16_bf16 v[48:63], v[188:191], v[6:9], v[48:63]
	ds_read_b128 v[188:191], v0 offset:13856
	v_mfma_f32_32x32x16_bf16 v[16:31], v[198:201], v[6:9], v[16:31]
	v_cvt_pk_f32_fp8_e32 v[6:7], v180
	v_cvt_pk_f32_fp8_sdwa v[8:9], v180 src0_sel:WORD_1
	v_cvt_pk_bf16_f32 v6, v6, v7
	v_cvt_pk_bf16_f32 v7, v8, v9
	v_cvt_pk_bf16_f32 v8, v10, v11
	v_cvt_pk_bf16_f32 v9, v12, v13
	ds_read_b128 v[10:13], v0 offset:4640
	s_waitcnt lgkmcnt(2)
	v_mfma_f32_32x32x16_bf16 v[128:143], v[2:5], v[6:9], v[128:143]
	s_waitcnt lgkmcnt(0)
	v_mfma_f32_32x32x16_bf16 v[96:111], v[10:13], v[6:9], v[96:111]
	v_mfma_f32_32x32x16_bf16 v[112:127], v[184:187], v[6:9], v[112:127]
	v_mfma_f32_32x32x16_bf16 v[80:95], v[188:191], v[6:9], v[80:95]
	v_cvt_pk_f32_fp8_e32 v[6:7], v176
	v_cvt_pk_f32_fp8_sdwa v[8:9], v176 src0_sel:WORD_1
	v_cvt_pk_f32_fp8_sdwa v[176:177], v177 src0_sel:WORD_1
	v_cvt_pk_bf16_f32 v6, v6, v7
	v_cvt_pk_bf16_f32 v7, v8, v9
	v_cvt_pk_bf16_f32 v8, v14, v15
	v_cvt_pk_bf16_f32 v9, v176, v177
	v_cvt_pk_f32_fp8_e32 v[14:15], v179
	v_cvt_pk_f32_fp8_sdwa v[176:177], v179 src0_sel:WORD_1
	v_mfma_f32_32x32x16_bf16 v[64:79], v[2:5], v[6:9], v[64:79]
	ds_read_b128 v[2:5], v0 offset:48
	v_mfma_f32_32x32x16_bf16 v[32:47], v[10:13], v[6:9], v[32:47]
	v_cvt_pk_f32_fp8_e32 v[10:11], v183
	v_cvt_pk_f32_fp8_sdwa v[12:13], v183 src0_sel:WORD_1
	v_mfma_f32_32x32x16_bf16 v[48:63], v[184:187], v[6:9], v[48:63]
	ds_read_b128 v[184:187], v0 offset:13872
	v_mfma_f32_32x32x16_bf16 v[16:31], v[188:191], v[6:9], v[16:31]
	v_cvt_pk_f32_fp8_e32 v[6:7], v182
	v_cvt_pk_f32_fp8_sdwa v[8:9], v182 src0_sel:WORD_1
	ds_read_b128 v[180:183], v0 offset:9264
	v_cvt_pk_bf16_f32 v6, v6, v7
	v_cvt_pk_bf16_f32 v7, v8, v9
	v_cvt_pk_bf16_f32 v8, v10, v11
	v_cvt_pk_bf16_f32 v9, v12, v13
	ds_read_b128 v[10:13], v0 offset:4656
	s_waitcnt lgkmcnt(3)
	v_mfma_f32_32x32x16_bf16 v[128:143], v[2:5], v[6:9], v[128:143]
	s_waitcnt lgkmcnt(0)
	v_mfma_f32_32x32x16_bf16 v[96:111], v[10:13], v[6:9], v[96:111]
	v_mfma_f32_32x32x16_bf16 v[112:127], v[180:183], v[6:9], v[112:127]
	v_mfma_f32_32x32x16_bf16 v[80:95], v[184:187], v[6:9], v[80:95]
	v_cvt_pk_f32_fp8_e32 v[6:7], v178
	v_cvt_pk_f32_fp8_sdwa v[8:9], v178 src0_sel:WORD_1
	v_cvt_pk_bf16_f32 v6, v6, v7
	v_cvt_pk_bf16_f32 v7, v8, v9
	v_cvt_pk_bf16_f32 v8, v14, v15
	v_cvt_pk_bf16_f32 v9, v176, v177
	s_nop 1
	v_mfma_f32_32x32x16_bf16 v[64:79], v[2:5], v[6:9], v[64:79]
	v_mfma_f32_32x32x16_bf16 v[32:47], v[10:13], v[6:9], v[32:47]
	v_mfma_f32_32x32x16_bf16 v[48:63], v[180:183], v[6:9], v[48:63]
	v_mfma_f32_32x32x16_bf16 v[16:31], v[184:187], v[6:9], v[16:31]
.LBB0_1326:
	s_add_i32 s25, s39, 1
	v_mov_b32_e32 v0, v194
	s_cmp_lg_u32 s39, 2
	s_cselect_b32 s29, s25, 0
	global_load_dwordx4 v[6:9], v0, s[46:47] offset:16
	global_load_dwordx4 v[176:179], v0, s[46:47]
	v_mov_b32_e32 v0, v195
	s_add_i32 s39, s49, 2
	s_mul_i32 s25, s29, 0x4800
	s_cmp_lt_u32 s39, s40
	global_load_dwordx4 v[2:5], v0, s[46:47] offset:16
	global_load_dwordx4 v[10:13], v0, s[46:47]
	v_add_u32_e32 v0, s25, v196
	s_cselect_b32 s25, s39, 0
	s_lshr_b32 s46, s25, 4
	s_add_i32 s46, s46, s76
	s_and_b32 s46, s46, s77
	s_add_i32 s46, s46, s27
	s_lshl_b32 s25, s25, 14
	s_lshl_b32 s46, s46, 6
	s_and_b32 s25, s25, 0x38000
	s_add_i32 s56, s46, s25
	s_waitcnt vmcnt(10)
	v_cvt_pk_bf16_f32 v14, v160, v164
	s_waitcnt vmcnt(8)
	v_cvt_pk_bf16_f32 v15, v168, v172
	s_lshl_b64 s[46:47], s[56:57], 2
	s_waitcnt lgkmcnt(0)
	s_barrier
	ds_write2_b32 v0, v14, v15 offset1:8
	v_cvt_pk_bf16_f32 v14, v161, v165
	v_cvt_pk_bf16_f32 v15, v169, v173
	v_add_u32_e32 v160, 0x400, v0
	s_add_u32 s46, s11, s46
	ds_write2_b32 v160, v14, v15 offset0:32 offset1:40
	v_cvt_pk_bf16_f32 v14, v162, v166
	v_cvt_pk_bf16_f32 v15, v170, v174
	v_add_u32_e32 v160, 0x800, v0
	s_addc_u32 s47, s79, s47
	ds_write2_b32 v160, v14, v15 offset0:64 offset1:72
	v_cvt_pk_bf16_f32 v14, v163, v167
	v_cvt_pk_bf16_f32 v15, v171, v175
	v_add_u32_e32 v0, 0xc00, v0
	s_add_u32 s90, s46, 0x4000
	ds_write2_b32 v0, v14, v15 offset0:96 offset1:104
	s_addc_u32 s91, s47, 0
	v_mov_b32_e32 v0, v192
	global_load_dwordx4 v[160:163], v0, s[46:47] nt
	global_load_dwordx4 v[164:167], v0, s[46:47] offset:1024 nt
	global_load_dwordx4 v[168:171], v0, s[90:91] nt
	global_load_dwordx4 v[172:175], v0, s[90:91] offset:1024 nt
	s_cmp_ge_u32 s49, s40
	s_cselect_b64 s[46:47], -1, 0
	s_and_b32 s25, s2, 0x380
	s_cmp_lt_u32 s49, s40
	s_cselect_b32 s25, s25, 0
	s_add_u32 s90, s25, s54
	s_addc_u32 s91, 0, s55
	s_and_b64 vcc, exec, s[0:1]
	s_cbranch_vccnz .LBB0_1328
	s_waitcnt vmcnt(6)
	v_cvt_pk_f32_fp8_sdwa v[186:187], v176 src0_sel:WORD_1
	v_cvt_pk_f32_fp8_e32 v[188:189], v177
	v_add_u32_e32 v0, s26, v232
	ds_read_b128 v[180:183], v0
	v_cvt_pk_bf16_f32 v185, v186, v187
	v_cvt_pk_bf16_f32 v186, v188, v189
	ds_read_b128 v[188:191], v0 offset:4608
	ds_read_b128 v[198:201], v0 offset:9216
	ds_read_b128 v[202:205], v0 offset:13824
	v_cvt_pk_f32_fp8_e32 v[14:15], v176
	v_cvt_pk_f32_fp8_sdwa v[176:177], v177 src0_sel:WORD_1
	v_cvt_pk_bf16_f32 v184, v14, v15
	v_cvt_pk_bf16_f32 v187, v176, v177
	s_waitcnt vmcnt(4)
	v_cvt_pk_f32_fp8_e32 v[14:15], v10
	v_cvt_pk_f32_fp8_sdwa v[176:177], v10 src0_sel:WORD_1
	s_waitcnt lgkmcnt(3)
	v_mfma_f32_32x32x16_bf16 v[128:143], v[180:183], v[184:187], v[128:143]
	s_waitcnt lgkmcnt(2)
	v_mfma_f32_32x32x16_bf16 v[96:111], v[188:191], v[184:187], v[96:111]
	s_waitcnt lgkmcnt(1)
	v_mfma_f32_32x32x16_bf16 v[112:127], v[198:201], v[184:187], v[112:127]
	s_waitcnt lgkmcnt(0)
	v_mfma_f32_32x32x16_bf16 v[80:95], v[202:205], v[184:187], v[80:95]
	v_cvt_pk_f32_fp8_e32 v[186:187], v11
	v_cvt_pk_f32_fp8_sdwa v[10:11], v11 src0_sel:WORD_1
	v_cvt_pk_bf16_f32 v184, v14, v15
	v_cvt_pk_bf16_f32 v185, v176, v177
	v_cvt_pk_bf16_f32 v186, v186, v187
	v_cvt_pk_bf16_f32 v187, v10, v11
	v_cvt_pk_f32_fp8_e32 v[10:11], v178
	v_cvt_pk_f32_fp8_sdwa v[14:15], v178 src0_sel:WORD_1
	v_mfma_f32_32x32x16_bf16 v[64:79], v[180:183], v[184:187], v[64:79]
	ds_read_b128 v[180:183], v0 offset:16
	v_cvt_pk_bf16_f32 v176, v10, v11
	v_cvt_pk_bf16_f32 v177, v14, v15
	v_cvt_pk_f32_fp8_e32 v[10:11], v12
	v_cvt_pk_f32_fp8_sdwa v[14:15], v12 src0_sel:WORD_1
	v_cvt_pk_bf16_f32 v10, v10, v11
	v_mfma_f32_32x32x16_bf16 v[32:47], v[188:191], v[184:187], v[32:47]
	ds_read_b128 v[188:191], v0 offset:9232
	v_cvt_pk_bf16_f32 v11, v14, v15
	v_cvt_pk_f32_fp8_e32 v[14:15], v7
	v_mfma_f32_32x32x16_bf16 v[48:63], v[198:201], v[184:187], v[48:63]
	ds_read_b128 v[198:201], v0 offset:13840
	v_mfma_f32_32x32x16_bf16 v[16:31], v[202:205], v[184:187], v[16:31]
	v_cvt_pk_f32_fp8_e32 v[184:185], v179
	v_cvt_pk_f32_fp8_sdwa v[186:187], v179 src0_sel:WORD_1
	v_cvt_pk_bf16_f32 v178, v184, v185
	v_cvt_pk_bf16_f32 v179, v186, v187
	ds_read_b128 v[184:187], v0 offset:4624
	s_waitcnt lgkmcnt(3)
	v_mfma_f32_32x32x16_bf16 v[128:143], v[180:183], v[176:179], v[128:143]
	s_waitcnt lgkmcnt(0)
	v_mfma_f32_32x32x16_bf16 v[96:111], v[184:187], v[176:179], v[96:111]
	v_mfma_f32_32x32x16_bf16 v[112:127], v[188:191], v[176:179], v[112:127]
	v_mfma_f32_32x32x16_bf16 v[80:95], v[198:201], v[176:179], v[80:95]
	v_cvt_pk_f32_fp8_e32 v[176:177], v13
	v_cvt_pk_f32_fp8_sdwa v[178:179], v13 src0_sel:WORD_1
	v_cvt_pk_bf16_f32 v12, v176, v177
	v_cvt_pk_bf16_f32 v13, v178, v179
	ds_read_b128 v[176:179], v0 offset:32
	s_nop 0
	v_mfma_f32_32x32x16_bf16 v[64:79], v[180:183], v[10:13], v[64:79]
	ds_read_b128 v[180:183], v0 offset:4640
	v_mfma_f32_32x32x16_bf16 v[32:47], v[184:187], v[10:13], v[32:47]
	ds_read_b128 v[184:187], v0 offset:9248
	v_mfma_f32_32x32x16_bf16 v[48:63], v[188:191], v[10:13], v[48:63]
	ds_read_b128 v[188:191], v0 offset:13856
	v_mfma_f32_32x32x16_bf16 v[16:31], v[198:201], v[10:13], v[16:31]
	v_cvt_pk_f32_fp8_e32 v[10:11], v6
	v_cvt_pk_f32_fp8_sdwa v[12:13], v6 src0_sel:WORD_1
	v_cvt_pk_f32_fp8_sdwa v[6:7], v7 src0_sel:WORD_1
	v_cvt_pk_bf16_f32 v10, v10, v11
	v_cvt_pk_bf16_f32 v11, v12, v13
	v_cvt_pk_bf16_f32 v12, v14, v15
	v_cvt_pk_bf16_f32 v13, v6, v7
	v_cvt_pk_f32_fp8_e32 v[6:7], v2
	v_cvt_pk_f32_fp8_e32 v[14:15], v3
	s_waitcnt lgkmcnt(3)
	v_mfma_f32_32x32x16_bf16 v[128:143], v[176:179], v[10:13], v[128:143]
	s_waitcnt lgkmcnt(2)
	v_mfma_f32_32x32x16_bf16 v[96:111], v[180:183], v[10:13], v[96:111]
	s_waitcnt lgkmcnt(1)
	v_mfma_f32_32x32x16_bf16 v[112:127], v[184:187], v[10:13], v[112:127]
	s_waitcnt lgkmcnt(0)
	v_mfma_f32_32x32x16_bf16 v[80:95], v[188:191], v[10:13], v[80:95]
	v_cvt_pk_f32_fp8_sdwa v[12:13], v2 src0_sel:WORD_1
	v_cvt_pk_f32_fp8_sdwa v[2:3], v3 src0_sel:WORD_1
	v_cvt_pk_bf16_f32 v10, v6, v7
	v_cvt_pk_bf16_f32 v11, v12, v13
	v_cvt_pk_bf16_f32 v12, v14, v15
	v_cvt_pk_bf16_f32 v13, v2, v3
	v_cvt_pk_f32_fp8_e32 v[2:3], v8
	v_cvt_pk_f32_fp8_sdwa v[14:15], v9 src0_sel:WORD_1
	v_mfma_f32_32x32x16_bf16 v[64:79], v[176:179], v[10:13], v[64:79]
	ds_read_b128 v[176:179], v0 offset:48
	v_cvt_pk_bf16_f32 v6, v2, v3
	v_cvt_pk_f32_fp8_e32 v[2:3], v4
	v_cvt_pk_bf16_f32 v2, v2, v3
	v_mfma_f32_32x32x16_bf16 v[32:47], v[180:183], v[10:13], v[32:47]
	ds_read_b128 v[180:183], v0 offset:9264
	v_mfma_f32_32x32x16_bf16 v[48:63], v[184:187], v[10:13], v[48:63]
	ds_read_b128 v[184:187], v0 offset:13872
	v_mfma_f32_32x32x16_bf16 v[16:31], v[188:191], v[10:13], v[16:31]
	v_cvt_pk_f32_fp8_sdwa v[10:11], v8 src0_sel:WORD_1
	v_cvt_pk_f32_fp8_e32 v[12:13], v9
	v_cvt_pk_bf16_f32 v9, v14, v15
	v_cvt_pk_f32_fp8_sdwa v[14:15], v5 src0_sel:WORD_1
	v_cvt_pk_bf16_f32 v7, v10, v11
	v_cvt_pk_bf16_f32 v8, v12, v13
	ds_read_b128 v[10:13], v0 offset:4656
	s_waitcnt lgkmcnt(3)
	v_mfma_f32_32x32x16_bf16 v[128:143], v[176:179], v[6:9], v[128:143]
	s_waitcnt lgkmcnt(0)
	v_mfma_f32_32x32x16_bf16 v[96:111], v[10:13], v[6:9], v[96:111]
	v_mfma_f32_32x32x16_bf16 v[112:127], v[180:183], v[6:9], v[112:127]
	v_mfma_f32_32x32x16_bf16 v[80:95], v[184:187], v[6:9], v[80:95]
	v_cvt_pk_f32_fp8_sdwa v[6:7], v4 src0_sel:WORD_1
	v_cvt_pk_f32_fp8_e32 v[8:9], v5
	v_cvt_pk_bf16_f32 v5, v14, v15
	v_cvt_pk_bf16_f32 v3, v6, v7
	v_cvt_pk_bf16_f32 v4, v8, v9
	s_nop 1
	v_mfma_f32_32x32x16_bf16 v[64:79], v[176:179], v[2:5], v[64:79]
	v_mfma_f32_32x32x16_bf16 v[32:47], v[10:13], v[2:5], v[32:47]
	v_mfma_f32_32x32x16_bf16 v[48:63], v[180:183], v[2:5], v[48:63]
	v_mfma_f32_32x32x16_bf16 v[16:31], v[184:187], v[2:5], v[16:31]

.LBB0_1430:
	v_or_b32_e32 v244, v0, v232
	s_mov_b64 s[42:43], s[50:51]
	s_mov_b64 s[64:65], s[48:49]
	v_mov_b32_e32 v0, v239
	global_load_dwordx4 v[200:203], v244, s[30:31] offset:16
	global_load_dwordx4 v[196:199], v244, s[30:31]
	global_load_dwordx4 v[2:5], v0, s[64:65] nt
	global_load_dwordx4 v[10:13], v0, s[42:43] nt
	v_lshl_add_u64 v[6:7], s[64:65], 0, v[0:1]
	v_add_co_u32_e32 v6, vcc, s85, v6
	v_lshl_add_u64 v[14:15], s[42:43], 0, v[0:1]
	s_nop 0
	v_addc_co_u32_e32 v7, vcc, 0, v7, vcc
	v_add_co_u32_e32 v14, vcc, s85, v14
	global_load_dwordx4 v[6:9], v[6:7], off nt
	s_nop 0
	v_addc_co_u32_e32 v15, vcc, 0, v15, vcc
	global_load_dwordx4 v[14:17], v[14:15], off nt
	s_mov_b64 s[42:43], s[52:53]
	s_mov_b64 s[64:65], s[54:55]
	v_mov_b32_e32 v0, v239
	global_load_dwordx4 v[160:163], v0, s[42:43] nt
	global_load_dwordx4 v[168:171], v0, s[64:65] nt
	v_lshl_add_u64 v[18:19], s[42:43], 0, v[0:1]
	v_add_co_u32_e32 v18, vcc, s85, v18
	v_add_u32_e32 v245, 0, v240
	s_nop 0
	v_addc_co_u32_e32 v19, vcc, 0, v19, vcc
	global_load_dwordx4 v[164:167], v[18:19], off nt
	v_lshl_add_u64 v[18:19], s[64:65], 0, v[0:1]
	v_add_co_u32_e32 v18, vcc, s85, v18
	s_mov_b64 s[42:43], s[60:61]
	s_nop 0
	v_addc_co_u32_e32 v19, vcc, 0, v19, vcc
	s_mov_b64 s[64:65], s[58:59]
	global_load_dwordx4 v[172:175], v[18:19], off nt
	s_min_i32 s45, s56, 0x400
	s_sub_i32 s25, s45, s84
	s_cmp_lt_i32 s33, s25
	v_add_u32_e32 v246, 0, v241
	s_mov_b32 s87, 0
	v_add_u32_e32 v247, s38, v246
	s_movk_i32 s45, 0x80
	s_mov_b32 s88, 2
	s_waitcnt vmcnt(5)
	v_cvt_pk_bf16_f32 v0, v2, v6
	v_mov_b32_e32 v6, v1
	s_waitcnt vmcnt(4)
	v_cvt_pk_bf16_f32 v2, v10, v14
	ds_write2_b32 v245, v0, v2 offset1:8
	v_cvt_pk_bf16_f32 v0, v3, v7
	v_cvt_pk_bf16_f32 v2, v11, v15
	v_add_u32_e32 v3, 0x400, v245
	ds_write2_b32 v3, v0, v2 offset0:32 offset1:40
	v_cvt_pk_bf16_f32 v0, v4, v8
	v_cvt_pk_bf16_f32 v2, v12, v16
	v_add_u32_e32 v3, 0x800, v245
	ds_write2_b32 v3, v0, v2 offset0:64 offset1:72
	v_cvt_pk_bf16_f32 v0, v5, v9
	v_cvt_pk_bf16_f32 v2, v13, v17
	v_add_u32_e32 v3, 0xc00, v245
	ds_write2_b32 v3, v0, v2 offset0:96 offset1:104
	v_mov_b32_e32 v0, v239
	global_load_dwordx4 v[176:179], v0, s[64:65] nt
	global_load_dwordx4 v[184:187], v0, s[42:43] nt
	v_lshl_add_u64 v[2:3], s[64:65], 0, v[0:1]
	v_add_co_u32_e32 v2, vcc, s85, v2
	v_mov_b32_e32 v14, v1
	s_nop 0
	v_addc_co_u32_e32 v3, vcc, 0, v3, vcc
	global_load_dwordx4 v[180:183], v[2:3], off nt
	v_lshl_add_u64 v[2:3], s[42:43], 0, v[0:1]
	v_add_co_u32_e32 v2, vcc, s85, v2
	v_mov_b32_e32 v15, v1
	s_nop 0
	v_addc_co_u32_e32 v3, vcc, 0, v3, vcc
	global_load_dwordx4 v[188:191], v[2:3], off nt
	s_cselect_b64 s[64:65], -1, 0
	v_mov_b32_e32 v0, v1
	v_mov_b32_e32 v2, v1
	v_mov_b32_e32 v3, v1
	v_mov_b32_e32 v4, v1
	v_mov_b32_e32 v5, v1
	v_mov_b32_e32 v7, v1
	v_mov_b32_e32 v8, v1
	v_mov_b32_e32 v9, v1
	v_mov_b32_e32 v10, v1
	v_mov_b32_e32 v11, v1
	v_mov_b32_e32 v12, v1
	v_mov_b32_e32 v13, v1
	v_mov_b32_e32 v16, 0
	s_cmp_lt_i32 s39, s25
	v_mov_b64_e32 v[46:47], v[14:15]
	v_mov_b64_e32 v[62:63], v[14:15]
	v_mov_b64_e32 v[78:79], v[14:15]
	v_mov_b64_e32 v[94:95], v[14:15]
	v_mov_b64_e32 v[110:111], v[14:15]
	v_mov_b64_e32 v[126:127], v[14:15]
	v_mov_b64_e32 v[142:143], v[14:15]
	v_mov_b64_e32 v[158:159], v[14:15]
	s_cselect_b64 s[66:67], -1, 0
	v_mov_b64_e32 v[44:45], v[12:13]
	v_mov_b64_e32 v[42:43], v[10:11]
	v_mov_b64_e32 v[40:41], v[8:9]
	v_mov_b64_e32 v[38:39], v[6:7]
	v_mov_b64_e32 v[36:37], v[4:5]
	v_mov_b64_e32 v[34:35], v[2:3]
	v_mov_b64_e32 v[32:33], v[0:1]
	v_mov_b64_e32 v[60:61], v[12:13]
	v_mov_b64_e32 v[58:59], v[10:11]
	v_mov_b64_e32 v[56:57], v[8:9]
	v_mov_b64_e32 v[54:55], v[6:7]
	v_mov_b64_e32 v[52:53], v[4:5]
	v_mov_b64_e32 v[50:51], v[2:3]
	v_mov_b64_e32 v[48:49], v[0:1]
	v_mov_b64_e32 v[76:77], v[12:13]
	v_mov_b64_e32 v[74:75], v[10:11]
	v_mov_b64_e32 v[72:73], v[8:9]
	v_mov_b64_e32 v[70:71], v[6:7]
	v_mov_b64_e32 v[68:69], v[4:5]
	v_mov_b64_e32 v[66:67], v[2:3]
	v_mov_b64_e32 v[64:65], v[0:1]
	v_mov_b64_e32 v[92:93], v[12:13]
	v_mov_b64_e32 v[90:91], v[10:11]
	v_mov_b64_e32 v[88:89], v[8:9]
	v_mov_b64_e32 v[86:87], v[6:7]
	v_mov_b64_e32 v[84:85], v[4:5]
	v_mov_b64_e32 v[82:83], v[2:3]
	v_mov_b64_e32 v[80:81], v[0:1]
	v_mov_b64_e32 v[108:109], v[12:13]
	v_mov_b64_e32 v[106:107], v[10:11]
	v_mov_b64_e32 v[104:105], v[8:9]
	v_mov_b64_e32 v[102:103], v[6:7]
	v_mov_b64_e32 v[100:101], v[4:5]
	v_mov_b64_e32 v[98:99], v[2:3]
	v_mov_b64_e32 v[96:97], v[0:1]
	v_mov_b64_e32 v[124:125], v[12:13]
	v_mov_b64_e32 v[122:123], v[10:11]
	v_mov_b64_e32 v[120:121], v[8:9]
	v_mov_b64_e32 v[118:119], v[6:7]
	v_mov_b64_e32 v[116:117], v[4:5]
	v_mov_b64_e32 v[114:115], v[2:3]
	v_mov_b64_e32 v[112:113], v[0:1]
	v_mov_b64_e32 v[140:141], v[12:13]
	v_mov_b64_e32 v[138:139], v[10:11]
	v_mov_b64_e32 v[136:137], v[8:9]
	v_mov_b64_e32 v[134:135], v[6:7]
	v_mov_b64_e32 v[132:133], v[4:5]
	v_mov_b64_e32 v[130:131], v[2:3]
	v_mov_b64_e32 v[128:129], v[0:1]
	v_mov_b64_e32 v[156:157], v[12:13]
	v_mov_b64_e32 v[154:155], v[10:11]
	v_mov_b64_e32 v[152:153], v[8:9]
	v_mov_b64_e32 v[150:151], v[6:7]
	v_mov_b64_e32 v[148:149], v[4:5]
	v_mov_b64_e32 v[146:147], v[2:3]
	v_mov_b64_e32 v[144:145], v[0:1]
	v_mov_b32_e32 v17, v16
	v_mov_b32_e32 v18, v16
	v_mov_b32_e32 v19, v16
	v_mov_b32_e32 v20, v16
	v_mov_b32_e32 v21, v16
	v_mov_b32_e32 v22, v16
	v_mov_b32_e32 v23, v16
	v_mov_b32_e32 v24, v16
	v_mov_b32_e32 v25, v16
	v_mov_b32_e32 v26, v16
	v_mov_b32_e32 v27, v16
	v_mov_b32_e32 v28, v16
	v_mov_b32_e32 v29, v16
	v_mov_b32_e32 v30, v16
	v_mov_b32_e32 v31, v16
	s_branch .LBB0_1433

.LBB0_1433:
	s_add_i32 s25, s87, 1
	s_cmp_lg_u32 s87, 2
	s_cselect_b32 s70, s25, 0
	s_mul_i32 s25, s70, 0x4800
	s_add_i32 s90, s25, 0
	s_add_i32 s25, s88, 1
	s_cmp_lt_u32 s25, s80
	s_cselect_b32 s25, s25, 0
	s_lshr_b32 s42, s25, 2
	s_add_i32 s42, s42, s79
	s_and_b32 s42, s42, s78
	s_add_i32 s42, s42, s77
	s_lshl_b32 s25, s25, 16
	s_lshl_b32 s42, s42, 7
	s_and_b32 s25, s25, 0x30000
	s_add_i32 s56, s42, s25
	v_add_u32_e32 v0, s90, v240
	s_waitcnt vmcnt(5)
	v_cvt_pk_bf16_f32 v2, v160, v164
	s_waitcnt vmcnt(4)
	v_cvt_pk_bf16_f32 v3, v168, v172
	s_lshl_b64 s[42:43], s[56:57], 2
	s_waitcnt lgkmcnt(0)
	s_barrier
	ds_write2_b32 v0, v2, v3 offset1:8
	v_cvt_pk_bf16_f32 v2, v161, v165
	v_cvt_pk_bf16_f32 v3, v169, v173
	v_add_u32_e32 v4, 0x400, v0
	s_add_u32 s42, s82, s42
	ds_write2_b32 v4, v2, v3 offset0:32 offset1:40
	v_cvt_pk_bf16_f32 v2, v162, v166
	v_cvt_pk_bf16_f32 v3, v170, v174
	v_add_u32_e32 v4, 0x800, v0
	s_addc_u32 s43, s83, s43
	ds_write2_b32 v4, v2, v3 offset0:64 offset1:72
	v_cvt_pk_bf16_f32 v2, v163, v167
	v_cvt_pk_bf16_f32 v3, v171, v175
	v_add_u32_e32 v0, 0xc00, v0
	s_add_u32 s68, s42, 0x10000
	ds_write2_b32 v0, v2, v3 offset0:96 offset1:104
	s_addc_u32 s69, s43, 0
	v_mov_b32_e32 v0, v239
	global_load_dwordx4 v[160:163], v0, s[42:43] nt
	global_load_dwordx4 v[168:171], v0, s[68:69] nt
	v_lshl_add_u64 v[2:3], s[42:43], 0, v[0:1]
	v_add_co_u32_e32 v2, vcc, s85, v2
	s_sub_i32 s42, s45, 64
	s_nop 0
	v_addc_co_u32_e32 v3, vcc, 0, v3, vcc
	global_load_dwordx4 v[164:167], v[2:3], off nt
	v_lshl_add_u64 v[2:3], s[68:69], 0, v[0:1]
	v_add_co_u32_e32 v2, vcc, s85, v2
	s_add_i32 s25, s88, -1
	s_nop 0
	v_addc_co_u32_e32 v3, vcc, 0, v3, vcc
	global_load_dwordx4 v[172:175], v[2:3], off nt
	s_and_b32 s42, s42, 0xc0
	s_cmp_lt_u32 s25, s80
	s_cselect_b32 s25, s42, 0
	s_add_u32 s68, s25, s30
	v_cndmask_b32_e64 v0, 0, 1, s[64:65]
	s_addc_u32 s69, 0, s31
	s_mul_i32 s56, s87, 0x4800
	v_cmp_ne_u32_e64 s[42:43], 1, v0
	s_andn2_b64 vcc, exec, s[64:65]
	s_cbranch_vccnz .LBB0_1435
	v_cvt_pk_f32_fp8_e32 v[6:7], v212
	v_cvt_pk_f32_fp8_sdwa v[8:9], v212 src0_sel:WORD_1
	v_cvt_pk_f32_fp8_e32 v[10:11], v213
	v_cvt_pk_f32_fp8_sdwa v[12:13], v213 src0_sel:WORD_1
	v_add_u32_e32 v0, s56, v246
	ds_read_b128 v[2:5], v0
	v_cvt_pk_bf16_f32 v6, v6, v7
	v_cvt_pk_bf16_f32 v7, v8, v9
	v_cvt_pk_bf16_f32 v8, v10, v11
	v_cvt_pk_bf16_f32 v9, v12, v13
	ds_read_b128 v[10:13], v0 offset:4608
	ds_read_b128 v[216:219], v0 offset:9216
	ds_read_b128 v[248:251], v0 offset:13824
	s_waitcnt lgkmcnt(3)
	v_mfma_f32_32x32x16_bf16 v[144:159], v[2:5], v[6:9], v[144:159]
	s_waitcnt vmcnt(6)
	v_cvt_pk_f32_fp8_e32 v[14:15], v209
	s_waitcnt lgkmcnt(2)
	v_mfma_f32_32x32x16_bf16 v[128:143], v[10:13], v[6:9], v[128:143]
	s_waitcnt lgkmcnt(1)
	v_mfma_f32_32x32x16_bf16 v[112:127], v[216:219], v[6:9], v[112:127]
	s_waitcnt lgkmcnt(0)
	v_mfma_f32_32x32x16_bf16 v[96:111], v[248:251], v[6:9], v[96:111]
	v_cvt_pk_f32_fp8_e32 v[6:7], v208
	v_cvt_pk_f32_fp8_sdwa v[8:9], v208 src0_sel:WORD_1
	v_cvt_pk_f32_fp8_sdwa v[208:209], v209 src0_sel:WORD_1
	v_cvt_pk_bf16_f32 v6, v6, v7
	v_cvt_pk_bf16_f32 v7, v8, v9
	v_cvt_pk_bf16_f32 v8, v14, v15
	v_cvt_pk_bf16_f32 v9, v208, v209
	v_cvt_pk_f32_fp8_e32 v[14:15], v211
	v_cvt_pk_f32_fp8_sdwa v[208:209], v211 src0_sel:WORD_1
	v_mfma_f32_32x32x16_bf16 v[80:95], v[2:5], v[6:9], v[80:95]
	ds_read_b128 v[2:5], v0 offset:16
	v_mfma_f32_32x32x16_bf16 v[64:79], v[10:13], v[6:9], v[64:79]
	v_cvt_pk_f32_fp8_e32 v[10:11], v215
	v_cvt_pk_f32_fp8_sdwa v[12:13], v215 src0_sel:WORD_1
	v_mfma_f32_32x32x16_bf16 v[48:63], v[216:219], v[6:9], v[48:63]
	ds_read_b128 v[216:219], v0 offset:13840
	v_mfma_f32_32x32x16_bf16 v[32:47], v[248:251], v[6:9], v[32:47]
	v_cvt_pk_f32_fp8_e32 v[6:7], v214
	v_cvt_pk_f32_fp8_sdwa v[8:9], v214 src0_sel:WORD_1
	ds_read_b128 v[212:215], v0 offset:9232
	v_cvt_pk_bf16_f32 v6, v6, v7
	v_cvt_pk_bf16_f32 v7, v8, v9
	v_cvt_pk_bf16_f32 v8, v10, v11
	v_cvt_pk_bf16_f32 v9, v12, v13
	ds_read_b128 v[10:13], v0 offset:4624
	s_waitcnt lgkmcnt(3)
	v_mfma_f32_32x32x16_bf16 v[144:159], v[2:5], v[6:9], v[144:159]
	s_waitcnt lgkmcnt(0)
	v_mfma_f32_32x32x16_bf16 v[128:143], v[10:13], v[6:9], v[128:143]
	v_mfma_f32_32x32x16_bf16 v[112:127], v[212:215], v[6:9], v[112:127]
	v_mfma_f32_32x32x16_bf16 v[96:111], v[216:219], v[6:9], v[96:111]
	v_cvt_pk_f32_fp8_e32 v[6:7], v210
	v_cvt_pk_f32_fp8_sdwa v[8:9], v210 src0_sel:WORD_1
	v_cvt_pk_bf16_f32 v6, v6, v7
	v_cvt_pk_bf16_f32 v7, v8, v9
	v_cvt_pk_bf16_f32 v8, v14, v15
	v_cvt_pk_bf16_f32 v9, v208, v209
	ds_read_b128 v[208:211], v0 offset:9248
	v_cvt_pk_f32_fp8_e32 v[14:15], v193
	v_mfma_f32_32x32x16_bf16 v[80:95], v[2:5], v[6:9], v[80:95]
	ds_read_b128 v[2:5], v0 offset:32
	v_mfma_f32_32x32x16_bf16 v[64:79], v[10:13], v[6:9], v[64:79]
	v_cvt_pk_f32_fp8_e32 v[10:11], v205
	v_cvt_pk_f32_fp8_sdwa v[12:13], v205 src0_sel:WORD_1
	v_mfma_f32_32x32x16_bf16 v[48:63], v[212:215], v[6:9], v[48:63]
	ds_read_b128 v[212:215], v0 offset:13856
	v_mfma_f32_32x32x16_bf16 v[32:47], v[216:219], v[6:9], v[32:47]
	v_cvt_pk_f32_fp8_e32 v[6:7], v204
	v_cvt_pk_f32_fp8_sdwa v[8:9], v204 src0_sel:WORD_1
	v_cvt_pk_bf16_f32 v6, v6, v7
	v_cvt_pk_bf16_f32 v7, v8, v9
	v_cvt_pk_bf16_f32 v8, v10, v11
	v_cvt_pk_bf16_f32 v9, v12, v13
	ds_read_b128 v[10:13], v0 offset:4640
	s_waitcnt lgkmcnt(2)
	v_mfma_f32_32x32x16_bf16 v[144:159], v[2:5], v[6:9], v[144:159]
	s_waitcnt lgkmcnt(0)
	v_mfma_f32_32x32x16_bf16 v[128:143], v[10:13], v[6:9], v[128:143]
	v_mfma_f32_32x32x16_bf16 v[112:127], v[208:211], v[6:9], v[112:127]
	v_mfma_f32_32x32x16_bf16 v[96:111], v[212:215], v[6:9], v[96:111]
	v_cvt_pk_f32_fp8_e32 v[6:7], v192
	v_cvt_pk_f32_fp8_sdwa v[8:9], v192 src0_sel:WORD_1
	v_cvt_pk_f32_fp8_sdwa v[192:193], v193 src0_sel:WORD_1
	v_cvt_pk_bf16_f32 v6, v6, v7
	v_cvt_pk_bf16_f32 v7, v8, v9
	v_cvt_pk_bf16_f32 v8, v14, v15
	v_cvt_pk_bf16_f32 v9, v192, v193
	v_cvt_pk_f32_fp8_e32 v[14:15], v195
	v_cvt_pk_f32_fp8_sdwa v[192:193], v195 src0_sel:WORD_1
	v_mfma_f32_32x32x16_bf16 v[80:95], v[2:5], v[6:9], v[80:95]
	ds_read_b128 v[2:5], v0 offset:48
	v_mfma_f32_32x32x16_bf16 v[64:79], v[10:13], v[6:9], v[64:79]
	v_cvt_pk_f32_fp8_e32 v[10:11], v207
	v_cvt_pk_f32_fp8_sdwa v[12:13], v207 src0_sel:WORD_1
	v_mfma_f32_32x32x16_bf16 v[48:63], v[208:211], v[6:9], v[48:63]
	ds_read_b128 v[208:211], v0 offset:13872
	v_mfma_f32_32x32x16_bf16 v[32:47], v[212:215], v[6:9], v[32:47]
	v_cvt_pk_f32_fp8_e32 v[6:7], v206
	v_cvt_pk_f32_fp8_sdwa v[8:9], v206 src0_sel:WORD_1
	ds_read_b128 v[204:207], v0 offset:9264
	v_cvt_pk_bf16_f32 v6, v6, v7
	v_cvt_pk_bf16_f32 v7, v8, v9
	v_cvt_pk_bf16_f32 v8, v10, v11
	v_cvt_pk_bf16_f32 v9, v12, v13
	ds_read_b128 v[10:13], v0 offset:4656
	s_waitcnt lgkmcnt(3)
	v_mfma_f32_32x32x16_bf16 v[144:159], v[2:5], v[6:9], v[144:159]
	s_waitcnt lgkmcnt(0)
	v_mfma_f32_32x32x16_bf16 v[128:143], v[10:13], v[6:9], v[128:143]
	v_mfma_f32_32x32x16_bf16 v[112:127], v[204:207], v[6:9], v[112:127]
	v_mfma_f32_32x32x16_bf16 v[96:111], v[208:211], v[6:9], v[96:111]
	v_cvt_pk_f32_fp8_e32 v[6:7], v194
	v_cvt_pk_f32_fp8_sdwa v[8:9], v194 src0_sel:WORD_1
	v_cvt_pk_bf16_f32 v6, v6, v7
	v_cvt_pk_bf16_f32 v7, v8, v9
	v_cvt_pk_bf16_f32 v8, v14, v15
	v_cvt_pk_bf16_f32 v9, v192, v193
	s_nop 1
	v_mfma_f32_32x32x16_bf16 v[80:95], v[2:5], v[6:9], v[80:95]
	v_mfma_f32_32x32x16_bf16 v[64:79], v[10:13], v[6:9], v[64:79]
	v_mfma_f32_32x32x16_bf16 v[48:63], v[204:207], v[6:9], v[48:63]
	v_mfma_f32_32x32x16_bf16 v[32:47], v[208:211], v[6:9], v[32:47]
.LBB0_1435:
	v_mov_b32_e32 v0, v242
	s_waitcnt vmcnt(5)
	v_cvt_pk_f32_fp8_e32 v[2:3], v196
	v_cvt_pk_f32_fp8_sdwa v[4:5], v196 src0_sel:WORD_1
	v_cvt_pk_f32_fp8_e32 v[10:11], v197
	v_cvt_pk_f32_fp8_sdwa v[12:13], v197 src0_sel:WORD_1
	global_load_dwordx4 v[192:195], v0, s[68:69] offset:16
	global_load_dwordx4 v[208:211], v0, s[68:69]
	v_mov_b32_e32 v0, v243
	global_load_dwordx4 v[6:9], v0, s[68:69] offset:16
	global_load_dwordx4 v[204:207], v0, s[68:69]
	v_add_u32_e32 v0, s56, v247
	v_cvt_pk_bf16_f32 v2, v2, v3
	v_cvt_pk_bf16_f32 v3, v4, v5
	v_cvt_pk_bf16_f32 v4, v10, v11
	v_cvt_pk_bf16_f32 v5, v12, v13
	ds_read_b128 v[10:13], v0
	v_cvt_pk_f32_fp8_sdwa v[14:15], v199 src0_sel:WORD_1
	s_waitcnt lgkmcnt(0)
	v_mfma_f32_32x32x16_bf16 v[16:31], v[10:13], v[2:5], v[16:31]
	v_cvt_pk_f32_fp8_e32 v[2:3], v198
	v_cvt_pk_f32_fp8_sdwa v[4:5], v198 src0_sel:WORD_1
	v_cvt_pk_f32_fp8_e32 v[12:13], v199
	s_add_i32 s25, s70, 1
	v_cvt_pk_bf16_f32 v10, v2, v3
	v_mov_b32_e32 v2, v244
	v_cvt_pk_bf16_f32 v11, v4, v5
	global_load_dwordx4 v[2:5], v2, s[68:69]
	ds_read_b128 v[196:199], v0 offset:16
	ds_read_b128 v[212:215], v0 offset:32
	v_cvt_pk_bf16_f32 v12, v12, v13
	v_cvt_pk_bf16_f32 v13, v14, v15
	s_waitcnt vmcnt(9)
	v_cvt_pk_f32_fp8_e32 v[14:15], v201
	s_cmp_lg_u32 s70, 2
	s_waitcnt lgkmcnt(1)
	v_mfma_f32_32x32x16_bf16 v[16:31], v[196:199], v[10:13], v[16:31]
	v_cvt_pk_f32_fp8_e32 v[10:11], v200
	v_cvt_pk_f32_fp8_sdwa v[12:13], v200 src0_sel:WORD_1
	v_cvt_pk_f32_fp8_sdwa v[196:197], v201 src0_sel:WORD_1
	v_cvt_pk_f32_fp8_sdwa v[200:201], v203 src0_sel:WORD_1
	v_cvt_pk_bf16_f32 v10, v10, v11
	v_cvt_pk_bf16_f32 v11, v12, v13
	v_cvt_pk_bf16_f32 v12, v14, v15
	v_cvt_pk_bf16_f32 v13, v196, v197
	s_cselect_b32 s87, s25, 0
	s_add_i32 s89, s88, 2
	s_waitcnt lgkmcnt(0)
	v_mfma_f32_32x32x16_bf16 v[16:31], v[212:215], v[10:13], v[16:31]
	v_cvt_pk_f32_fp8_e32 v[10:11], v202
	s_mul_i32 s25, s87, 0x4800
	s_cmp_lt_u32 s89, s80
	v_cvt_pk_f32_fp8_sdwa v[12:13], v202 src0_sel:WORD_1
	v_cvt_pk_bf16_f32 v196, v10, v11
	v_mov_b32_e32 v10, v244
	v_cvt_pk_f32_fp8_e32 v[14:15], v203
	v_cvt_pk_bf16_f32 v199, v200, v201
	ds_read_b128 v[200:203], v0 offset:48
	v_add_u32_e32 v0, s25, v245
	s_cselect_b32 s25, s89, 0
	s_lshr_b32 s56, s25, 2
	s_add_i32 s56, s56, s79
	s_and_b32 s56, s56, s78
	s_add_i32 s56, s56, s77
	s_lshl_b32 s25, s25, 16
	s_lshl_b32 s56, s56, 7
	s_and_b32 s25, s25, 0x20000
	s_add_i32 s56, s56, s25
	v_cvt_pk_bf16_f32 v197, v12, v13
	v_cvt_pk_bf16_f32 v198, v14, v15
	global_load_dwordx4 v[10:13], v10, s[68:69] offset:16
	s_waitcnt vmcnt(11)
	v_cvt_pk_bf16_f32 v14, v176, v180
	s_waitcnt vmcnt(10)
	v_cvt_pk_bf16_f32 v15, v184, v188
	s_lshl_b64 s[68:69], s[56:57], 2
	s_waitcnt lgkmcnt(0)
	s_barrier
	ds_write2_b32 v0, v14, v15 offset1:8
	v_cvt_pk_bf16_f32 v14, v177, v181
	v_cvt_pk_bf16_f32 v15, v185, v189
	v_add_u32_e32 v176, 0x400, v0
	s_add_u32 s68, s82, s68
	ds_write2_b32 v176, v14, v15 offset0:32 offset1:40
	v_cvt_pk_bf16_f32 v14, v178, v182
	v_cvt_pk_bf16_f32 v15, v186, v190
	v_add_u32_e32 v176, 0x800, v0
	s_addc_u32 s69, s83, s69
	ds_write2_b32 v176, v14, v15 offset0:64 offset1:72
	v_cvt_pk_bf16_f32 v14, v179, v183
	v_cvt_pk_bf16_f32 v15, v187, v191
	v_add_u32_e32 v0, 0xc00, v0
	s_add_u32 s70, s68, 0x10000
	ds_write2_b32 v0, v14, v15 offset0:96 offset1:104
	s_addc_u32 s71, s69, 0
	v_mov_b32_e32 v0, v239
	global_load_dwordx4 v[176:179], v0, s[68:69] nt
	global_load_dwordx4 v[184:187], v0, s[70:71] nt
	v_lshl_add_u64 v[14:15], s[68:69], 0, v[0:1]
	v_add_co_u32_e32 v14, vcc, s85, v14
	v_mfma_f32_32x32x16_bf16 v[16:31], v[200:203], v[196:199], v[16:31]
	s_nop 0
	v_addc_co_u32_e32 v15, vcc, 0, v15, vcc
	global_load_dwordx4 v[180:183], v[14:15], off nt
	v_lshl_add_u64 v[14:15], s[70:71], 0, v[0:1]
	v_add_co_u32_e32 v14, vcc, s85, v14
	s_cmp_ge_u32 s88, s80
	s_nop 0
	v_addc_co_u32_e32 v15, vcc, 0, v15, vcc
	global_load_dwordx4 v[188:191], v[14:15], off nt
	s_cselect_b64 s[68:69], -1, 0
	s_and_b32 s25, s45, 0x80
	s_cmp_lt_u32 s88, s80
	s_cselect_b32 s25, s25, 0
	s_add_u32 s70, s25, s30
	s_addc_u32 s71, 0, s31
	s_and_b64 vcc, exec, s[42:43]
	s_cbranch_vccnz .LBB0_1437
	s_waitcnt vmcnt(8)
	v_cvt_pk_f32_fp8_sdwa v[202:203], v208 src0_sel:WORD_1
	v_cvt_pk_f32_fp8_e32 v[212:213], v209
	v_add_u32_e32 v0, s90, v241
	ds_read_b128 v[196:199], v0
	v_cvt_pk_bf16_f32 v201, v202, v203
	v_cvt_pk_bf16_f32 v202, v212, v213
	ds_read_b128 v[212:215], v0 offset:4608
	ds_read_b128 v[216:219], v0 offset:9216
	ds_read_b128 v[248:251], v0 offset:13824
	v_cvt_pk_f32_fp8_e32 v[14:15], v208
	v_cvt_pk_f32_fp8_sdwa v[208:209], v209 src0_sel:WORD_1
	v_cvt_pk_bf16_f32 v200, v14, v15
	v_cvt_pk_bf16_f32 v203, v208, v209
	s_waitcnt vmcnt(6)
	v_cvt_pk_f32_fp8_e32 v[14:15], v204
	v_cvt_pk_f32_fp8_e32 v[208:209], v205
	s_waitcnt lgkmcnt(3)
	v_mfma_f32_32x32x16_bf16 v[144:159], v[196:199], v[200:203], v[144:159]
	s_waitcnt lgkmcnt(2)
	v_mfma_f32_32x32x16_bf16 v[128:143], v[212:215], v[200:203], v[128:143]
	s_waitcnt lgkmcnt(1)
	v_mfma_f32_32x32x16_bf16 v[112:127], v[216:219], v[200:203], v[112:127]
	s_waitcnt lgkmcnt(0)
	v_mfma_f32_32x32x16_bf16 v[96:111], v[248:251], v[200:203], v[96:111]
	v_cvt_pk_f32_fp8_sdwa v[202:203], v204 src0_sel:WORD_1
	v_cvt_pk_f32_fp8_sdwa v[204:205], v205 src0_sel:WORD_1
	v_cvt_pk_bf16_f32 v200, v14, v15
	v_cvt_pk_f32_fp8_e32 v[14:15], v210
	v_cvt_pk_bf16_f32 v201, v202, v203
	v_cvt_pk_bf16_f32 v202, v208, v209
	v_cvt_pk_bf16_f32 v203, v204, v205
	v_cvt_pk_f32_fp8_sdwa v[208:209], v211 src0_sel:WORD_1
	v_cvt_pk_f32_fp8_e32 v[204:205], v211
	v_mfma_f32_32x32x16_bf16 v[80:95], v[196:199], v[200:203], v[80:95]
	ds_read_b128 v[196:199], v0 offset:16
	v_mfma_f32_32x32x16_bf16 v[64:79], v[212:215], v[200:203], v[64:79]
	ds_read_b128 v[212:215], v0 offset:9232
	v_mfma_f32_32x32x16_bf16 v[48:63], v[216:219], v[200:203], v[48:63]
	ds_read_b128 v[216:219], v0 offset:13840
	v_mfma_f32_32x32x16_bf16 v[32:47], v[248:251], v[200:203], v[32:47]
	v_cvt_pk_f32_fp8_sdwa v[202:203], v210 src0_sel:WORD_1
	v_cvt_pk_bf16_f32 v200, v14, v15
	v_cvt_pk_f32_fp8_e32 v[14:15], v206
	v_cvt_pk_bf16_f32 v201, v202, v203
	v_cvt_pk_bf16_f32 v203, v208, v209
	ds_read_b128 v[208:211], v0 offset:4624
	v_cvt_pk_bf16_f32 v202, v204, v205
	v_cvt_pk_f32_fp8_e32 v[204:205], v207
	s_waitcnt lgkmcnt(3)
	v_mfma_f32_32x32x16_bf16 v[144:159], v[196:199], v[200:203], v[144:159]
	s_waitcnt lgkmcnt(0)
	v_mfma_f32_32x32x16_bf16 v[128:143], v[208:211], v[200:203], v[128:143]
	v_mfma_f32_32x32x16_bf16 v[112:127], v[212:215], v[200:203], v[112:127]
	v_mfma_f32_32x32x16_bf16 v[96:111], v[216:219], v[200:203], v[96:111]
	v_cvt_pk_f32_fp8_sdwa v[202:203], v206 src0_sel:WORD_1
	v_cvt_pk_f32_fp8_sdwa v[206:207], v207 src0_sel:WORD_1
	v_cvt_pk_bf16_f32 v200, v14, v15
	v_cvt_pk_f32_fp8_e32 v[14:15], v192
	v_cvt_pk_bf16_f32 v201, v202, v203
	v_cvt_pk_bf16_f32 v202, v204, v205
	v_cvt_pk_bf16_f32 v203, v206, v207
	v_cvt_pk_f32_fp8_e32 v[204:205], v193
	s_nop 0
	v_mfma_f32_32x32x16_bf16 v[80:95], v[196:199], v[200:203], v[80:95]
	ds_read_b128 v[196:199], v0 offset:32
	v_mfma_f32_32x32x16_bf16 v[64:79], v[208:211], v[200:203], v[64:79]
	ds_read_b128 v[208:211], v0 offset:9248
	v_mfma_f32_32x32x16_bf16 v[48:63], v[212:215], v[200:203], v[48:63]
	ds_read_b128 v[212:215], v0 offset:13856
	v_mfma_f32_32x32x16_bf16 v[32:47], v[216:219], v[200:203], v[32:47]
	v_cvt_pk_f32_fp8_sdwa v[202:203], v192 src0_sel:WORD_1
	v_cvt_pk_f32_fp8_sdwa v[192:193], v193 src0_sel:WORD_1
	v_cvt_pk_bf16_f32 v200, v14, v15
	v_cvt_pk_f32_fp8_e32 v[14:15], v6
	v_cvt_pk_bf16_f32 v201, v202, v203
	v_cvt_pk_bf16_f32 v202, v204, v205
	ds_read_b128 v[204:207], v0 offset:4640
	v_cvt_pk_bf16_f32 v203, v192, v193
	v_cvt_pk_f32_fp8_sdwa v[192:193], v6 src0_sel:WORD_1
	s_waitcnt lgkmcnt(3)
	v_mfma_f32_32x32x16_bf16 v[144:159], v[196:199], v[200:203], v[144:159]
	s_waitcnt lgkmcnt(0)
	v_mfma_f32_32x32x16_bf16 v[128:143], v[204:207], v[200:203], v[128:143]
	v_mfma_f32_32x32x16_bf16 v[112:127], v[208:211], v[200:203], v[112:127]
	v_mfma_f32_32x32x16_bf16 v[96:111], v[212:215], v[200:203], v[96:111]
	v_cvt_pk_f32_fp8_e32 v[202:203], v7
	v_cvt_pk_f32_fp8_sdwa v[6:7], v7 src0_sel:WORD_1
	v_cvt_pk_bf16_f32 v200, v14, v15
	v_cvt_pk_bf16_f32 v201, v192, v193
	v_cvt_pk_bf16_f32 v202, v202, v203
	v_cvt_pk_bf16_f32 v203, v6, v7
	v_cvt_pk_f32_fp8_e32 v[6:7], v194
	v_cvt_pk_f32_fp8_sdwa v[14:15], v194 src0_sel:WORD_1
	v_mfma_f32_32x32x16_bf16 v[80:95], v[196:199], v[200:203], v[80:95]
	ds_read_b128 v[196:199], v0 offset:48
	v_cvt_pk_bf16_f32 v192, v6, v7
	v_cvt_pk_bf16_f32 v193, v14, v15
	v_cvt_pk_f32_fp8_e32 v[6:7], v8
	v_cvt_pk_f32_fp8_sdwa v[14:15], v8 src0_sel:WORD_1
	v_cvt_pk_bf16_f32 v6, v6, v7
	v_mfma_f32_32x32x16_bf16 v[64:79], v[204:207], v[200:203], v[64:79]
	ds_read_b128 v[204:207], v0 offset:9264
	v_cvt_pk_bf16_f32 v7, v14, v15
	v_mfma_f32_32x32x16_bf16 v[48:63], v[208:211], v[200:203], v[48:63]
	ds_read_b128 v[208:211], v0 offset:13872
	v_mfma_f32_32x32x16_bf16 v[32:47], v[212:215], v[200:203], v[32:47]
	v_cvt_pk_f32_fp8_e32 v[200:201], v195
	v_cvt_pk_f32_fp8_sdwa v[202:203], v195 src0_sel:WORD_1
	v_cvt_pk_bf16_f32 v194, v200, v201
	v_cvt_pk_bf16_f32 v195, v202, v203
	ds_read_b128 v[200:203], v0 offset:4656
	s_waitcnt lgkmcnt(3)
	v_mfma_f32_32x32x16_bf16 v[144:159], v[196:199], v[192:195], v[144:159]
	s_waitcnt lgkmcnt(0)
	v_mfma_f32_32x32x16_bf16 v[128:143], v[200:203], v[192:195], v[128:143]
	v_mfma_f32_32x32x16_bf16 v[112:127], v[204:207], v[192:195], v[112:127]
	v_mfma_f32_32x32x16_bf16 v[96:111], v[208:211], v[192:195], v[96:111]
	v_cvt_pk_f32_fp8_e32 v[192:193], v9
	v_cvt_pk_f32_fp8_sdwa v[194:195], v9 src0_sel:WORD_1
	v_cvt_pk_bf16_f32 v8, v192, v193
	v_cvt_pk_bf16_f32 v9, v194, v195
	s_nop 1
	v_mfma_f32_32x32x16_bf16 v[80:95], v[196:199], v[6:9], v[80:95]
	v_mfma_f32_32x32x16_bf16 v[64:79], v[200:203], v[6:9], v[64:79]
	v_mfma_f32_32x32x16_bf16 v[48:63], v[204:207], v[6:9], v[48:63]
	v_mfma_f32_32x32x16_bf16 v[32:47], v[208:211], v[6:9], v[32:47]
